# v7
# speedup vs baseline: 1.0089x; 1.0042x over previous
.LBB6_41:
	s_or_b64 exec, exec, s[0:1]
	v_lshlrev_b32_e32 v0, 3, v55
	v_lshl_or_b32 v0, v56, 8, v0
	v_add_u32_e32 v0, 0x1800, v0
	s_waitcnt lgkmcnt(0)
	s_barrier
	ds_read2_b64 v[38:41], v0 offset0:32 offset1:48
	v_or_b32_e32 v0, v1, v54
	v_lshl_add_u32 v1, v56, 5, s28
	v_or_b32_e32 v81, v1, v55
	v_lshlrev_b32_e32 v80, 2, v0
	v_mad_i64_i32 v[42:43], s[0:1], v81, s13, 0
	v_lshl_add_u64 v[74:75], v[42:43], 1, s[24:25]
	ds_read_b128 v[42:45], v80 offset:4096
	ds_read_b128 v[46:49], v80 offset:4672
	ds_read_b128 v[50:53], v80 offset:5248
	ds_read_b128 v[54:57], v80 offset:5824
	ds_read_b128 v[58:61], v80 offset:4160
	ds_read_b128 v[62:65], v80 offset:4224
	s_waitcnt lgkmcnt(4)
	v_pk_add_f32 v[76:77], v[42:43], v[46:47]
	v_pk_add_f32 v[78:79], v[44:45], v[48:49]
	s_waitcnt lgkmcnt(2)
	v_pk_add_f32 v[54:55], v[50:51], v[54:55]
	v_pk_fma_f32 v[34:35], v[38:39], v[76:77], v[34:35] op_sel_hi:[0,1,1] neg_lo:[1,0,0] neg_hi:[1,0,0]
	v_pk_fma_f32 v[34:35], v[38:39], v[34:35], v[54:55] op_sel:[1,0,0]
	v_pk_add_f32 v[56:57], v[52:53], v[56:57]
	v_pk_add_f32 v[34:35], v[10:11], v[34:35]
	ds_read_b128 v[66:69], v80 offset:5312
	ds_read_b128 v[70:73], v80 offset:5376
	v_cvt_pk_f16_f32 v88, v34, v35
	v_pk_fma_f32 v[34:35], v[38:39], v[78:79], v[36:37] op_sel_hi:[0,1,1] neg_lo:[1,0,0] neg_hi:[1,0,0]
	v_pk_fma_f32 v[34:35], v[38:39], v[34:35], v[56:57] op_sel:[1,0,0]
	v_add_u32_e32 v0, s10, v0
	v_pk_add_f32 v[34:35], v[12:13], v[34:35]
	ds_read_b128 v[42:45], v80 offset:5888
	ds_read_b128 v[50:53], v80 offset:5952
	v_cvt_pk_f16_f32 v89, v34, v35
	ds_read_b128 v[34:37], v80 offset:4736
	v_ashrrev_i32_e32 v1, 31, v0
	v_lshlrev_b64 v[0:1], 1, v[0:1]
	v_lshl_add_u64 v[74:75], v[74:75], 0, v[0:1]
	v_mbcnt_lo_u32_b32 v94, -1, 0
	v_mbcnt_hi_u32_b32 v94, -1, v94
	v_and_b32_e32 v94, 16, v94
	v_lshrrev_b32_e32 v95, 1, v94
	v_add_u32_e32 v94, v94, v95
	v_mov_b32_e32 v95, 0
	ds_read_b128 v[46:49], v80 offset:4800
	s_waitcnt lgkmcnt(1)
	v_pk_add_f32 v[34:35], v[58:59], v[34:35]
	v_pk_add_f32 v[36:37], v[60:61], v[36:37]
	v_pk_add_f32 v[42:43], v[66:67], v[42:43]
	v_pk_fma_f32 v[30:31], v[38:39], v[34:35], v[30:31] op_sel_hi:[0,1,1] neg_lo:[1,0,0] neg_hi:[1,0,0]
	v_pk_add_f32 v[44:45], v[68:69], v[44:45]
	v_pk_fma_f32 v[32:33], v[38:39], v[36:37], v[32:33] op_sel_hi:[0,1,1] neg_lo:[1,0,0] neg_hi:[1,0,0]
	v_pk_fma_f32 v[30:31], v[38:39], v[30:31], v[42:43] op_sel:[1,0,0]
	v_pk_fma_f32 v[32:33], v[38:39], v[32:33], v[44:45] op_sel:[1,0,0]
	v_pk_add_f32 v[30:31], v[6:7], v[30:31]
	v_pk_add_f32 v[32:33], v[8:9], v[32:33]
	v_cvt_pk_f16_f32 v90, v30, v31
	v_cvt_pk_f16_f32 v91, v32, v33
	v_lshl_add_u64 v[92:93], v[74:75], 0, v[94:95]
	s_nop 1
	v_permlane16_swap_b32 v88, v90
	v_permlane16_swap_b32 v89, v91
	global_store_dwordx4 v[92:93], v[88:91], off
	s_waitcnt lgkmcnt(0)
	v_pk_add_f32 v[30:31], v[62:63], v[46:47]
	v_pk_add_f32 v[46:47], v[64:65], v[48:49]
	v_pk_add_f32 v[32:33], v[70:71], v[50:51]
	v_pk_fma_f32 v[26:27], v[38:39], v[30:31], v[26:27] op_sel_hi:[0,1,1] neg_lo:[1,0,0] neg_hi:[1,0,0]
	v_pk_add_f32 v[48:49], v[72:73], v[52:53]
	v_pk_fma_f32 v[28:29], v[38:39], v[46:47], v[28:29] op_sel_hi:[0,1,1] neg_lo:[1,0,0] neg_hi:[1,0,0]
	v_pk_fma_f32 v[26:27], v[38:39], v[26:27], v[32:33] op_sel:[1,0,0]
	v_pk_fma_f32 v[28:29], v[38:39], v[28:29], v[48:49] op_sel:[1,0,0]
	v_pk_add_f32 v[26:27], v[2:3], v[26:27]
	v_pk_add_f32 v[28:29], v[4:5], v[28:29]
	v_pk_fma_f32 v[22:23], v[40:41], v[76:77], v[22:23] op_sel_hi:[0,1,1] neg_lo:[1,0,0] neg_hi:[1,0,0]
	v_cvt_pk_f16_f32 v26, v26, v27
	v_cvt_pk_f16_f32 v27, v28, v29
	v_pk_fma_f32 v[22:23], v[40:41], v[22:23], v[54:55] op_sel:[1,0,0]
	global_store_dwordx2 v[74:75], v[26:27], off offset:64
	v_or_b32_e32 v26, 16, v81
	v_pk_add_f32 v[10:11], v[10:11], v[22:23]
	v_pk_fma_f32 v[22:23], v[40:41], v[78:79], v[24:25] op_sel_hi:[0,1,1] neg_lo:[1,0,0] neg_hi:[1,0,0]
	v_mad_i64_i32 v[26:27], s[0:1], v26, s13, 0
	v_pk_fma_f32 v[22:23], v[40:41], v[22:23], v[56:57] op_sel:[1,0,0]
	v_lshl_add_u64 v[26:27], v[26:27], 1, s[24:25]
	v_pk_add_f32 v[12:13], v[12:13], v[22:23]
	v_cvt_pk_f16_f32 v96, v10, v11
	v_cvt_pk_f16_f32 v97, v12, v13
	v_lshl_add_u64 v[0:1], v[26:27], 0, v[0:1]
	v_pk_fma_f32 v[10:11], v[40:41], v[34:35], v[18:19] op_sel_hi:[0,1,1] neg_lo:[1,0,0] neg_hi:[1,0,0]
	v_pk_fma_f32 v[10:11], v[40:41], v[10:11], v[42:43] op_sel:[1,0,0]
	s_nop 0
	v_pk_add_f32 v[6:7], v[6:7], v[10:11]
	v_pk_fma_f32 v[10:11], v[40:41], v[36:37], v[20:21] op_sel_hi:[0,1,1] neg_lo:[1,0,0] neg_hi:[1,0,0]
	v_pk_fma_f32 v[10:11], v[40:41], v[10:11], v[44:45] op_sel:[1,0,0]
	v_cvt_pk_f16_f32 v98, v6, v7
	v_pk_add_f32 v[8:9], v[8:9], v[10:11]
	s_nop 0
	v_cvt_pk_f16_f32 v99, v8, v9
	v_lshl_add_u64 v[92:93], v[0:1], 0, v[94:95]
	s_nop 1
	v_permlane16_swap_b32 v96, v98
	v_permlane16_swap_b32 v97, v99
	global_store_dwordx4 v[92:93], v[96:99], off
	v_pk_fma_f32 v[6:7], v[40:41], v[30:31], v[14:15] op_sel_hi:[0,1,1] neg_lo:[1,0,0] neg_hi:[1,0,0]
	v_pk_fma_f32 v[6:7], v[40:41], v[6:7], v[32:33] op_sel:[1,0,0]
	s_nop 0
	v_pk_add_f32 v[2:3], v[2:3], v[6:7]
	v_pk_fma_f32 v[6:7], v[40:41], v[46:47], v[16:17] op_sel_hi:[0,1,1] neg_lo:[1,0,0] neg_hi:[1,0,0]
	v_pk_fma_f32 v[6:7], v[40:41], v[6:7], v[48:49] op_sel:[1,0,0]
	v_cvt_pk_f16_f32 v2, v2, v3
	v_pk_add_f32 v[4:5], v[4:5], v[6:7]
	s_nop 0
	v_cvt_pk_f16_f32 v3, v4, v5
	global_store_dwordx2 v[0:1], v[2:3], off offset:64
	s_endpgm
	.p2align	8

	.amdhsa_kernel _Z7gemm_tnILi128ELi144ELi4ELi3ELi4ELi7ELi1EEvPKDF16_S1_PKfPfPDF16_iiiiiS3_S3_S4_
		.amdhsa_group_segment_fixed_size 7424
		.amdhsa_private_segment_fixed_size 0
		.amdhsa_kernarg_size 88
		.amdhsa_user_sgpr_count 2
		.amdhsa_user_sgpr_dispatch_ptr 0
		.amdhsa_user_sgpr_queue_ptr 0
		.amdhsa_user_sgpr_kernarg_segment_ptr 1
		.amdhsa_user_sgpr_dispatch_id 0
		.amdhsa_user_sgpr_kernarg_preload_length 0
		.amdhsa_user_sgpr_kernarg_preload_offset 0
		.amdhsa_user_sgpr_private_segment_size 0
		.amdhsa_uses_dynamic_stack 0
		.amdhsa_enable_private_segment 0
		.amdhsa_system_sgpr_workgroup_id_x 1
		.amdhsa_system_sgpr_workgroup_id_y 0
		.amdhsa_system_sgpr_workgroup_id_z 0
		.amdhsa_system_sgpr_workgroup_info 0
		.amdhsa_system_vgpr_workitem_id 0
		.amdhsa_next_free_vgpr 100
		.amdhsa_next_free_sgpr 91
		.amdhsa_accum_offset 100
		.amdhsa_reserve_vcc 1
		.amdhsa_float_round_mode_32 0
		.amdhsa_float_round_mode_16_64 0
		.amdhsa_float_denorm_mode_32 3
		.amdhsa_float_denorm_mode_16_64 3
		.amdhsa_dx10_clamp 1
		.amdhsa_ieee_mode 1
		.amdhsa_fp16_overflow 0
		.amdhsa_tg_split 0
		.amdhsa_exception_fp_ieee_invalid_op 0
		.amdhsa_exception_fp_denorm_src 0
		.amdhsa_exception_fp_ieee_div_zero 0
		.amdhsa_exception_fp_ieee_overflow 0
		.amdhsa_exception_fp_ieee_underflow 0
		.amdhsa_exception_fp_ieee_inexact 0
		.amdhsa_exception_int_div_zero 0
	.end_amdhsa_kernel

.LBB8_4:
	s_abs_i32 s3, s15
	v_cvt_f32_u32_e32 v1, s3
	s_sub_i32 s18, 0, s3
	s_add_i32 s2, s10, s2
	s_abs_i32 s11, s2
	v_rcp_iflag_f32_e32 v1, v1
	s_xor_b32 s10, s2, s15
	s_ashr_i32 s10, s10, 31
	v_bfe_u32 v16, v0, 6, 2
	v_mul_f32_e32 v1, 0x4f7ffffe, v1
	v_cvt_u32_f32_e32 v1, v1
	v_bfe_u32 v17, v0, 4, 2
	v_mov_b32_e32 v15, 0
	v_readfirstlane_b32 s19, v1
	s_mul_i32 s18, s18, s19
	s_mul_hi_u32 s18, s19, s18
	s_add_i32 s19, s19, s18
	s_mul_hi_u32 s18, s11, s19
	s_mul_i32 s19, s18, s3
	s_sub_i32 s11, s11, s19
	s_add_i32 s20, s18, 1
	s_sub_i32 s19, s11, s3
	s_cmp_ge_u32 s11, s3
	s_cselect_b32 s18, s20, s18
	s_cselect_b32 s11, s19, s11
	s_add_i32 s19, s18, 1
	s_cmp_ge_u32 s11, s3
	s_cselect_b32 s3, s19, s18
	s_abs_i32 s11, s14
	v_cvt_f32_u32_e32 v1, s11
	s_xor_b32 s3, s3, s10
	s_sub_i32 s3, s3, s10
	s_mul_i32 s10, s3, s15
	v_rcp_iflag_f32_e32 v1, v1
	s_sub_i32 s25, s2, s10
	s_xor_b32 s2, s25, s14
	s_sub_i32 s18, 0, s11
	v_mul_f32_e32 v1, 0x4f7ffffe, v1
	v_cvt_u32_f32_e32 v1, v1
	s_ashr_i32 s24, s2, 31
	s_abs_i32 s10, s25
	v_readfirstlane_b32 s2, v1
	s_mul_i32 s18, s18, s2
	s_mul_hi_u32 s15, s2, s18
	s_add_i32 s2, s2, s15
	s_mul_hi_u32 s2, s10, s2
	s_mul_i32 s15, s2, s11
	s_sub_i32 s10, s10, s15
	s_add_i32 s18, s2, 1
	s_sub_i32 s15, s10, s11
	s_cmp_ge_u32 s10, s11
	s_cselect_b32 s2, s18, s2
	s_cselect_b32 s10, s15, s10
	s_add_i32 s15, s2, 1
	s_cmp_ge_u32 s10, s11
	s_cselect_b32 s2, s15, s2
	s_xor_b32 s27, s2, s24
	s_sub_i32 s28, s27, s24
	s_mul_i32 s29, s28, s14
	s_sub_i32 s2, s25, s29
	s_lshl_b32 s22, s2, 7
	s_ashr_i32 s2, s6, 31
	v_lshrrev_b32_e32 v1, 3, v0
	s_lshr_b32 s2, s2, 26
	v_mul_lo_u32 v2, s6, v1
	v_xor_b32_e32 v1, v1, v0
	s_add_i32 s2, s6, s2
	v_lshlrev_b32_e32 v1, 3, v1
	s_ashr_i32 s23, s2, 6
	s_mul_i32 s2, s4, s6
	v_and_b32_e32 v1, 56, v1
	s_lshl_b32 s10, s2, 1
	s_mul_i32 s2, s5, s6
	s_mul_i32 s30, s23, s3
	v_add_lshl_u32 v62, v2, v1, 1
	v_mov_b32_e32 v1, 0x2000
	s_lshl_b32 s14, s2, 1
	s_lshl_b32 s2, s30, 6
	v_lshl_add_u32 v63, v0, 4, v1
	s_mul_i32 s31, s22, s6
	s_add_i32 s19, s31, s2
	v_readfirstlane_b32 s20, v63
	v_readfirstlane_b32 s40, v63
	s_and_b32 s9, s9, 0xffff
	s_mov_b32 s11, 0x20000
	s_lshl_b32 s19, s19, 1
	s_mov_b32 m0, s20
	v_add_u32_e32 v1, 0x2000, v63
	buffer_load_dwordx4 v62, s[8:11], s19 offen lds
	s_lshl_b32 s19, s6, 6
	s_add_i32 s20, s31, s19
	s_mul_i32 s18, s28, 0xc0
	s_add_i32 s21, s20, s2
	v_readfirstlane_b32 s33, v1
	s_mul_i32 s3, s18, s6
	s_lshl_b32 s21, s21, 1
	s_mov_b32 m0, s33
	v_add_u32_e32 v1, 0x4000, v63
	buffer_load_dwordx4 v62, s[8:11], s21 offen lds
	s_add_i32 s21, s3, s2
	v_readfirstlane_b32 s33, v1
	s_and_b32 s13, s13, 0xffff
	s_mov_b32 s15, s11
	s_lshl_b32 s21, s21, 1
	s_mov_b32 m0, s33
	v_add_u32_e32 v1, 0x6000, v63
	buffer_load_dwordx4 v62, s[12:15], s21 offen lds
	s_add_i32 s21, s3, s19
	s_add_i32 s33, s21, s2
	v_readfirstlane_b32 s34, v1
	s_lshl_b32 s33, s33, 1
	s_mov_b32 m0, s34
	v_add_u32_e32 v1, 0x8000, v63
	s_add_i32 s19, s21, s19
	buffer_load_dwordx4 v62, s[12:15], s33 offen lds
	s_add_i32 s33, s19, s2
	v_readfirstlane_b32 s34, v1
	s_lshl_b32 s33, s33, 1
	s_mov_b32 m0, s34
	v_add_u32_e32 v1, 0xa000, v63
	s_add_i32 s2, s2, 64
	buffer_load_dwordx4 v62, s[12:15], s33 offen lds
	s_add_i32 s33, s31, s2
	v_readfirstlane_b32 s34, v1
	s_lshl_b32 s33, s33, 1
	s_mov_b32 m0, s34
	v_add_u32_e32 v1, 0xc000, v63
	buffer_load_dwordx4 v62, s[8:11], s33 offen lds
	s_add_i32 s20, s20, s2
	v_readfirstlane_b32 s33, v1
	s_lshl_b32 s20, s20, 1
	s_mov_b32 m0, s33
	v_add_u32_e32 v1, 0xe000, v63
	buffer_load_dwordx4 v62, s[8:11], s20 offen lds
	s_add_i32 s3, s3, s2
	v_readfirstlane_b32 s20, v1
	v_add_u32_e32 v1, 0x10000, v63
	s_lshl_b32 s3, s3, 1
	s_mov_b32 m0, s20
	s_add_i32 s21, s21, s2
	v_readfirstlane_b32 s20, v1
	buffer_load_dwordx4 v62, s[12:15], s3 offen lds
	s_lshl_b32 s3, s21, 1
	s_mov_b32 m0, s20
	v_add_u32_e32 v1, 0x12000, v63
	buffer_load_dwordx4 v62, s[12:15], s3 offen lds
	s_add_i32 s19, s19, s2
	v_readfirstlane_b32 s3, v1
	s_lshl_b32 s2, s19, 1
	s_mov_b32 m0, s3
	s_ashr_i32 s19, s18, 31
	buffer_load_dwordx4 v62, s[12:15], s2 offen lds
	s_lshl_b64 s[2:3], s[18:19], 2
	s_add_u32 s2, s16, s2
	v_mul_u32_u24_e32 v1, 48, v16
	s_addc_u32 s3, s17, s3
	v_lshlrev_b32_e32 v14, 2, v1
	v_lshl_add_u64 v[2:3], s[2:3], 0, v[14:15]
	v_lshlrev_b32_e32 v14, 4, v17
	v_lshl_add_u64 v[18:19], v[2:3], 0, v[14:15]
	global_load_dwordx4 v[10:13], v[18:19], off
	global_load_dwordx4 v[6:9], v[18:19], off offset:64
	global_load_dwordx4 v[2:5], v[18:19], off offset:128
	s_movk_i32 s2, 0x180
	v_cmp_gt_u32_e64 s[2:3], s2, v0
	s_and_saveexec_b64 s[16:17], s[2:3]
	s_cbranch_execz .LBB8_6
	s_load_dwordx4 s[36:39], s[0:1], 0x40
	v_subrev_co_u32_e32 v14, vcc, 0xc0, v0
	s_movk_i32 s15, 0xbf
	s_nop 0
	v_cndmask_b32_e32 v14, v14, v0, vcc
	v_cmp_lt_u32_e32 vcc, s15, v0
	v_lshl_add_u64 v[14:15], s[18:19], 0, v[14:15]
	s_nop 0
	v_cndmask_b32_e64 v22, 0, 3, vcc
	v_mad_i64_i32 v[18:19], s[20:21], s5, v22, v[14:15]
	v_lshlrev_b64 v[18:19], 2, v[18:19]
	s_waitcnt lgkmcnt(0)
	v_lshl_add_u64 v[20:21], s[36:37], 0, v[18:19]
	v_lshl_add_u64 v[18:19], s[38:39], 0, v[18:19]
	global_load_dword v74, v[18:19], off
	v_add_u32_e32 v18, 1, v22
	v_mad_i64_i32 v[18:19], s[20:21], s5, v18, v[14:15]
	v_lshlrev_b64 v[18:19], 2, v[18:19]
	global_load_dword v75, v[20:21], off
	v_lshl_add_u64 v[20:21], s[36:37], 0, v[18:19]
	v_lshl_add_u64 v[18:19], s[38:39], 0, v[18:19]
	global_load_dword v76, v[18:19], off
	v_add_u32_e32 v18, 2, v22
	v_mad_i64_i32 v[14:15], s[20:21], s5, v18, v[14:15]
	v_lshlrev_b64 v[14:15], 2, v[14:15]
	v_lshl_add_u64 v[18:19], s[36:37], 0, v[14:15]
	v_lshl_add_u64 v[14:15], s[38:39], 0, v[14:15]
	global_load_dword v78, v[20:21], off
	global_load_dword v79, v[18:19], off
	global_load_dword v77, v[14:15], off

.LBB8_18:
	s_waitcnt vmcnt(5)
	s_add_i32 s15, s26, 2
	s_cmp_ge_i32 s15, s23
	s_barrier
	s_cbranch_scc1 .LBB8_17
	s_mul_hi_u32 s15, s25, 0xaaaaaaab
	s_lshr_b32 s15, s15, 1
	s_mul_i32 s15, s15, 0x1e000
	s_sub_i32 s27, s24, s15
	s_add_i32 s41, s40, s27
	s_add_i32 s41, s41, 0x14000
	s_mov_b32 s15, s11
	s_add_i32 s42, s4, s7
	s_add_i32 s43, s19, s7
	s_add_i32 s44, s20, s7
	s_add_i32 s45, s21, s7
	s_add_i32 s46, s6, s7
	s_mul_hi_u32 s47, s26, 0xaaaaaaab
	s_lshr_b32 s47, s47, 1
	s_mul_i32 s47, s47, 0x1e000
	v_subrev_u32_e32 v90, s47, v87
	v_add_u32_e32 v114, s24, v85
	v_subrev_u32_e32 v94, s47, v89
	v_add_u32_e32 v106, v114, v90
	v_add_u32_e32 v115, v114, v94
	ds_read_b128 v[90:93], v106 offset:16384
	ds_read_b128 v[94:97], v115
	ds_read_b128 v[98:101], v106 offset:18432
	ds_read_b128 v[102:105], v115 offset:2048
	ds_read_b128 v[106:109], v106 offset:20480
	v_subrev_u32_e32 v110, s47, v88
	v_add_u32_e32 v116, v114, v110
	s_mov_b32 m0, s41
	s_add_i32 s26, s26, 1
	s_waitcnt lgkmcnt(2)
	v_mfma_f32_16x16x32_f16 v[58:61], v[98:101], v[94:97], v[58:61]
	ds_read_b128 v[110:113], v116
	s_add_i32 s24, s24, 0xa000
	s_add_i32 s25, s25, 1
	v_mfma_f32_16x16x32_f16 v[50:53], v[90:93], v[94:97], v[50:53]
	buffer_load_dwordx4 v62, s[8:11], s42 offen lds
	s_add_i32 s41, s41, 0x2000
	s_addk_i32 s7, 0x80
	s_waitcnt lgkmcnt(1)
	v_mfma_f32_16x16x32_f16 v[42:45], v[106:109], v[94:97], v[42:45]
	s_mov_b32 m0, s41
	v_mfma_f32_16x16x32_f16 v[46:49], v[90:93], v[102:105], v[46:49]
	v_mfma_f32_16x16x32_f16 v[38:41], v[98:101], v[102:105], v[38:41]
	buffer_load_dwordx4 v62, s[8:11], s43 offen lds
	s_add_i32 s41, s41, 0x2000
	v_mfma_f32_16x16x32_f16 v[34:37], v[106:109], v[102:105], v[34:37]
	ds_read_b128 v[94:97], v115 offset:4096
	ds_read_b128 v[102:105], v115 offset:6144
	s_mov_b32 m0, s41
	s_waitcnt lgkmcnt(1)
	v_mfma_f32_16x16x32_f16 v[30:33], v[90:93], v[94:97], v[30:33]
	s_waitcnt lgkmcnt(0)
	v_mfma_f32_16x16x32_f16 v[14:17], v[90:93], v[102:105], v[14:17]
	v_subrev_u32_e32 v90, s47, v86
	v_mfma_f32_16x16x32_f16 v[26:29], v[98:101], v[94:97], v[26:29]
	buffer_load_dwordx4 v62, s[12:15], s44 offen lds
	s_add_i32 s41, s41, 0x2000
	v_mfma_f32_16x16x32_f16 v[18:21], v[98:101], v[102:105], v[18:21]
	v_add_u32_e32 v98, v114, v90
	ds_read_b128 v[90:93], v98 offset:16384
	s_mov_b32 m0, s41
	v_mfma_f32_16x16x32_f16 v[22:25], v[106:109], v[94:97], v[22:25]
	ds_read_b128 v[94:97], v98 offset:18432
	ds_read_b128 v[98:101], v98 offset:20480
	v_mfma_f32_16x16x32_f16 v[54:57], v[106:109], v[102:105], v[54:57]
	ds_read_b128 v[102:105], v116 offset:2048
	ds_read_b128 v[106:109], v116 offset:4096
	buffer_load_dwordx4 v62, s[12:15], s45 offen lds
	s_add_i32 s41, s41, 0x2000
	s_waitcnt lgkmcnt(1)
	v_mfma_f32_16x16x32_f16 v[46:49], v[90:93], v[102:105], v[46:49]
	s_mov_b32 m0, s41
	v_mfma_f32_16x16x32_f16 v[38:41], v[94:97], v[102:105], v[38:41]
	v_mfma_f32_16x16x32_f16 v[34:37], v[98:101], v[102:105], v[34:37]
	ds_read_b128 v[102:105], v116 offset:6144
	v_mfma_f32_16x16x32_f16 v[50:53], v[90:93], v[110:113], v[50:53]
	buffer_load_dwordx4 v62, s[12:15], s46 offen lds
	v_mfma_f32_16x16x32_f16 v[58:61], v[94:97], v[110:113], v[58:61]
	v_mfma_f32_16x16x32_f16 v[42:45], v[98:101], v[110:113], v[42:45]
	s_waitcnt lgkmcnt(1)
	v_mfma_f32_16x16x32_f16 v[30:33], v[90:93], v[106:109], v[30:33]
	v_mfma_f32_16x16x32_f16 v[26:29], v[94:97], v[106:109], v[26:29]
	v_mfma_f32_16x16x32_f16 v[22:25], v[98:101], v[106:109], v[22:25]
	s_waitcnt lgkmcnt(0)
	v_mfma_f32_16x16x32_f16 v[14:17], v[90:93], v[102:105], v[14:17]
	v_mfma_f32_16x16x32_f16 v[18:21], v[94:97], v[102:105], v[18:21]
	s_cmp_eq_u32 s1, s26
	v_mfma_f32_16x16x32_f16 v[54:57], v[98:101], v[102:105], v[54:57]
	s_cbranch_scc1 .LBB8_20
	s_branch .LBB8_18

.LBB8_26:
	s_or_b64 exec, exec, s[0:1]
	v_lshlrev_b32_e32 v0, 3, v81
	v_lshl_or_b32 v0, v82, 9, v0
	v_add_u32_e32 v87, 0x1800, v0
	s_waitcnt lgkmcnt(0)
	s_barrier
	ds_read2_b64 v[50:53], v87 offset0:128 offset1:144
	v_or_b32_e32 v0, v1, v80
	v_lshlrev_b32_e32 v112, 2, v0
	v_lshl_add_u32 v1, v82, 6, s22
	v_or_b32_e32 v86, v1, v81
	ds_read_b128 v[70:73], v112 offset:4096
	ds_read_b128 v[76:79], v112 offset:4864
	ds_read_b128 v[80:83], v112 offset:5632
	ds_read_b128 v[88:91], v112 offset:6400
	ds_read_b128 v[92:95], v112 offset:4160
	ds_read_b128 v[96:99], v112 offset:4224
	v_add_u32_e32 v66, s18, v0
	v_mad_i64_i32 v[0:1], s[0:1], v86, s5, 0
	s_waitcnt lgkmcnt(4)
	v_pk_add_f32 v[76:77], v[70:71], v[76:77]
	v_lshl_add_u64 v[68:69], v[0:1], 1, s[16:17]
	s_waitcnt lgkmcnt(2)
	v_pk_add_f32 v[84:85], v[80:81], v[88:89]
	v_pk_fma_f32 v[0:1], v[50:51], v[76:77], v[38:39] op_sel_hi:[0,1,1] neg_lo:[1,0,0] neg_hi:[1,0,0]
	v_pk_fma_f32 v[0:1], v[50:51], v[0:1], v[84:85] op_sel:[1,0,0]
	s_mov_b32 s6, 0x3f3504f3
	v_pk_add_f32 v[0:1], v[10:11], v[0:1]
	s_mov_b32 s1, 0x3ea7ba05
	v_pk_mul_f32 v[38:39], v[0:1], s[6:7] op_sel_hi:[1,0]
	v_pk_mul_f32 v[80:81], v[0:1], 0.5 op_sel_hi:[1,0]
	v_fma_f32 v67, |v38|, s1, 1.0
	v_fma_f32 v0, |v39|, s1, 1.0
	v_rcp_f32_e32 v70, v67
	v_rcp_f32_e32 v71, v0
	v_mul_f32_e64 v67, |v38|, -|v38|
	v_mul_f32_e32 v67, 0x3fb8aa3b, v67
	s_mov_b32 s0, 0xbfba00e3
	v_exp_f32_e32 v74, v67
	s_mov_b32 s2, 0x3f87dc22
	v_mov_b64_e32 v[0:1], s[0:1]
	v_mul_f32_e64 v67, |v39|, -|v39|
	v_pk_fma_f32 v[88:89], v[70:71], s[2:3], v[0:1] op_sel_hi:[1,0,0]
	s_mov_b32 s8, 0x3fb5f0e3
	v_mul_f32_e32 v67, 0x3fb8aa3b, v67
	v_pk_fma_f32 v[88:89], v[70:71], v[88:89], s[8:9] op_sel_hi:[1,1,0]
	s_mov_b32 s0, 0xbe91a98e
	v_exp_f32_e32 v75, v67
	v_pk_fma_f32 v[88:89], v[70:71], v[88:89], s[0:1] op_sel_hi:[1,1,0]
	s_mov_b32 s4, 0x3e827906
	v_pk_fma_f32 v[88:89], v[70:71], v[88:89], s[4:5] op_sel_hi:[1,1,0]
	s_brev_b32 s3, -2
	v_pk_mul_f32 v[70:71], v[70:71], v[88:89]
	v_pk_add_f32 v[82:83], v[82:83], v[90:91]
	v_pk_fma_f32 v[70:71], v[74:75], v[70:71], 1.0 op_sel_hi:[1,1,0] neg_lo:[1,0,0] neg_hi:[1,0,0]
	ds_read_b128 v[100:103], v112 offset:5696
	ds_read_b128 v[104:107], v112 offset:5760
	v_bfi_b32 v39, s3, v71, v39
	v_bfi_b32 v38, s3, v70, v38
	v_pk_add_f32 v[38:39], v[38:39], 1.0 op_sel_hi:[1,0]
	ds_read_b128 v[88:91], v112 offset:4928
	ds_read_b128 v[108:111], v112 offset:4992
	v_pk_mul_f32 v[38:39], v[80:81], v[38:39]
	v_pk_add_f32 v[80:81], v[72:73], v[78:79]
	v_cvt_pk_f16_f32 v120, v38, v39
	v_pk_fma_f32 v[40:41], v[50:51], v[80:81], v[40:41] op_sel_hi:[0,1,1] neg_lo:[1,0,0] neg_hi:[1,0,0]
	v_pk_fma_f32 v[40:41], v[50:51], v[40:41], v[82:83] op_sel:[1,0,0]
	v_pk_fma_f32 v[54:55], v[52:53], v[76:77], v[54:55] op_sel_hi:[0,1,1] neg_lo:[1,0,0] neg_hi:[1,0,0]
	v_pk_add_f32 v[40:41], v[12:13], v[40:41]
	v_pk_fma_f32 v[54:55], v[52:53], v[54:55], v[84:85] op_sel:[1,0,0]
	v_pk_mul_f32 v[70:71], v[40:41], s[6:7] op_sel_hi:[1,0]
	v_pk_mul_f32 v[40:41], v[40:41], 0.5 op_sel_hi:[1,0]
	v_fma_f32 v39, |v70|, s1, 1.0
	v_fma_f32 v67, |v71|, s1, 1.0
	v_rcp_f32_e32 v72, v39
	v_rcp_f32_e32 v73, v67
	v_mul_f32_e64 v39, |v70|, -|v70|
	v_mul_f32_e32 v39, 0x3fb8aa3b, v39
	v_exp_f32_e32 v74, v39
	v_mul_f32_e64 v39, |v71|, -|v71|
	v_pk_fma_f32 v[78:79], v[72:73], s[2:3], v[0:1] op_sel_hi:[1,0,0]
	v_mul_f32_e32 v39, 0x3fb8aa3b, v39
	v_pk_fma_f32 v[78:79], v[72:73], v[78:79], s[8:9] op_sel_hi:[1,1,0]
	v_exp_f32_e32 v75, v39
	v_pk_fma_f32 v[78:79], v[72:73], v[78:79], s[0:1] op_sel_hi:[1,1,0]
	v_ashrrev_i32_e32 v67, 31, v66
	v_pk_fma_f32 v[78:79], v[72:73], v[78:79], s[4:5] op_sel_hi:[1,1,0]
	v_pk_add_f32 v[54:55], v[10:11], v[54:55]
	v_pk_mul_f32 v[72:73], v[72:73], v[78:79]
	v_pk_fma_f32 v[56:57], v[52:53], v[80:81], v[56:57] op_sel_hi:[0,1,1] neg_lo:[1,0,0] neg_hi:[1,0,0]
	v_pk_fma_f32 v[72:73], v[74:75], v[72:73], 1.0 op_sel_hi:[1,1,0] neg_lo:[1,0,0] neg_hi:[1,0,0]
	s_waitcnt lgkmcnt(1)
	v_pk_add_f32 v[74:75], v[92:93], v[88:89]
	v_bfi_b32 v71, s3, v73, v71
	v_bfi_b32 v70, s3, v72, v70
	v_pk_add_f32 v[70:71], v[70:71], 1.0 op_sel_hi:[1,0]
	v_lshlrev_b64 v[72:73], 1, v[66:67]
	v_pk_mul_f32 v[40:41], v[40:41], v[70:71]
	v_lshl_add_u64 v[116:117], v[68:69], 0, v[72:73]
	ds_read_b128 v[68:71], v112 offset:6464
	v_cvt_pk_f16_f32 v121, v40, v41
	v_mbcnt_lo_u32_b32 v118, -1, 0
	v_mbcnt_hi_u32_b32 v118, -1, v118
	v_bfe_u32 v137, v118, 4, 1
	v_and_b32_e32 v118, 16, v118
	v_lshrrev_b32_e32 v119, 1, v118
	v_add_u32_e32 v118, v118, v119
	v_mov_b32_e32 v119, 0
	v_mul_u32_u24_e32 v136, 0x17ff8, v137
	v_add_u32_e32 v136, 0xfffe8040, v136
	v_add_u32_e32 v137, -1, v137
	v_pk_fma_f32 v[38:39], v[50:51], v[74:75], v[62:63] op_sel_hi:[0,1,1] neg_lo:[1,0,0] neg_hi:[1,0,0]
	ds_read_b128 v[112:115], v112 offset:6528
	s_waitcnt lgkmcnt(1)
	v_pk_add_f32 v[78:79], v[100:101], v[68:69]
	v_pk_add_f32 v[70:71], v[102:103], v[70:71]
	v_pk_fma_f32 v[38:39], v[50:51], v[38:39], v[78:79] op_sel:[1,0,0]
	v_pk_fma_f32 v[56:57], v[52:53], v[56:57], v[82:83] op_sel:[1,0,0]
	v_pk_add_f32 v[62:63], v[6:7], v[38:39]
	v_pk_add_f32 v[56:57], v[12:13], v[56:57]
	v_pk_mul_f32 v[66:67], v[62:63], s[6:7] op_sel_hi:[1,0]
	v_pk_mul_f32 v[62:63], v[62:63], 0.5 op_sel_hi:[1,0]
	v_fma_f32 v38, |v66|, s1, 1.0
	v_fma_f32 v39, |v67|, s1, 1.0
	v_rcp_f32_e32 v38, v38
	v_rcp_f32_e32 v39, v39
	v_mul_f32_e64 v40, |v66|, -|v66|
	v_mul_f32_e32 v40, 0x3fb8aa3b, v40
	v_mul_f32_e64 v69, |v67|, -|v67|
	v_exp_f32_e32 v68, v40
	v_pk_fma_f32 v[40:41], v[38:39], s[2:3], v[0:1] op_sel_hi:[1,0,0]
	v_mul_f32_e32 v69, 0x3fb8aa3b, v69
	v_pk_fma_f32 v[40:41], v[38:39], v[40:41], s[8:9] op_sel_hi:[1,1,0]
	v_exp_f32_e32 v69, v69
	v_pk_fma_f32 v[40:41], v[38:39], v[40:41], s[0:1] op_sel_hi:[1,1,0]
	v_pk_fma_f32 v[46:47], v[52:53], v[74:75], v[46:47] op_sel_hi:[0,1,1] neg_lo:[1,0,0] neg_hi:[1,0,0]
	v_pk_fma_f32 v[40:41], v[38:39], v[40:41], s[4:5] op_sel_hi:[1,1,0]
	v_pk_fma_f32 v[46:47], v[52:53], v[46:47], v[78:79] op_sel:[1,0,0]
	v_pk_mul_f32 v[88:89], v[38:39], v[40:41]
	ds_read2_b64 v[38:41], v87 offset0:160 offset1:176
	v_pk_fma_f32 v[68:69], v[68:69], v[88:89], 1.0 op_sel_hi:[1,1,0] neg_lo:[1,0,0] neg_hi:[1,0,0]
	v_pk_add_f32 v[46:47], v[6:7], v[46:47]
	v_bfi_b32 v67, s3, v69, v67
	v_bfi_b32 v66, s3, v68, v66
	v_pk_add_f32 v[68:69], v[94:95], v[90:91]
	v_pk_add_f32 v[66:67], v[66:67], 1.0 op_sel_hi:[1,0]
	v_pk_fma_f32 v[64:65], v[50:51], v[68:69], v[64:65] op_sel_hi:[0,1,1] neg_lo:[1,0,0] neg_hi:[1,0,0]
	v_pk_fma_f32 v[64:65], v[50:51], v[64:65], v[70:71] op_sel:[1,0,0]
	v_pk_mul_f32 v[62:63], v[62:63], v[66:67]
	v_pk_add_f32 v[64:65], v[8:9], v[64:65]
	v_cvt_pk_f16_f32 v122, v62, v63
	v_pk_mul_f32 v[66:67], v[64:65], s[6:7] op_sel_hi:[1,0]
	v_pk_mul_f32 v[64:65], v[64:65], 0.5 op_sel_hi:[1,0]
	v_fma_f32 v63, |v66|, s1, 1.0
	v_fma_f32 v87, |v67|, s1, 1.0
	v_rcp_f32_e32 v88, v63
	v_rcp_f32_e32 v89, v87
	v_mul_f32_e64 v63, |v66|, -|v66|
	v_mul_f32_e32 v63, 0x3fb8aa3b, v63
	v_exp_f32_e32 v90, v63
	v_mul_f32_e64 v63, |v67|, -|v67|
	v_pk_fma_f32 v[92:93], v[88:89], s[2:3], v[0:1] op_sel_hi:[1,0,0]
	v_mul_f32_e32 v63, 0x3fb8aa3b, v63
	v_pk_fma_f32 v[92:93], v[88:89], v[92:93], s[8:9] op_sel_hi:[1,1,0]
	v_exp_f32_e32 v91, v63
	v_pk_fma_f32 v[92:93], v[88:89], v[92:93], s[0:1] op_sel_hi:[1,1,0]
	v_pk_fma_f32 v[48:49], v[52:53], v[68:69], v[48:49] op_sel_hi:[0,1,1] neg_lo:[1,0,0] neg_hi:[1,0,0]
	v_pk_fma_f32 v[92:93], v[88:89], v[92:93], s[4:5] op_sel_hi:[1,1,0]
	v_pk_fma_f32 v[48:49], v[52:53], v[48:49], v[70:71] op_sel:[1,0,0]
	v_pk_mul_f32 v[88:89], v[88:89], v[92:93]
	v_pk_add_f32 v[48:49], v[8:9], v[48:49]
	v_pk_fma_f32 v[88:89], v[90:91], v[88:89], 1.0 op_sel_hi:[1,1,0] neg_lo:[1,0,0] neg_hi:[1,0,0]
	s_waitcnt lgkmcnt(0)
	v_pk_fma_f32 v[34:35], v[38:39], v[76:77], v[34:35] op_sel_hi:[0,1,1] neg_lo:[1,0,0] neg_hi:[1,0,0]
	v_bfi_b32 v67, s3, v89, v67
	v_bfi_b32 v66, s3, v88, v66
	v_pk_add_f32 v[66:67], v[66:67], 1.0 op_sel_hi:[1,0]
	v_pk_fma_f32 v[34:35], v[38:39], v[34:35], v[84:85] op_sel:[1,0,0]
	v_pk_mul_f32 v[64:65], v[64:65], v[66:67]
	v_pk_add_f32 v[34:35], v[10:11], v[34:35]
	v_cvt_pk_f16_f32 v123, v64, v65
	v_lshl_add_u64 v[138:139], v[116:117], 0, v[118:119]
	s_nop 1
	v_permlane16_swap_b32 v120, v122
	v_permlane16_swap_b32 v121, v123
	global_store_dwordx4 v[138:139], v[120:123], off
	v_pk_add_f32 v[62:63], v[96:97], v[108:109]
	v_pk_add_f32 v[64:65], v[104:105], v[112:113]
	v_pk_fma_f32 v[58:59], v[50:51], v[62:63], v[58:59] op_sel_hi:[0,1,1] neg_lo:[1,0,0] neg_hi:[1,0,0]
	v_pk_fma_f32 v[58:59], v[50:51], v[58:59], v[64:65] op_sel:[1,0,0]
	v_pk_fma_f32 v[42:43], v[52:53], v[62:63], v[42:43] op_sel_hi:[0,1,1] neg_lo:[1,0,0] neg_hi:[1,0,0]
	v_pk_add_f32 v[58:59], v[2:3], v[58:59]
	v_pk_fma_f32 v[42:43], v[52:53], v[42:43], v[64:65] op_sel:[1,0,0]
	v_pk_mul_f32 v[66:67], v[58:59], s[6:7] op_sel_hi:[1,0]
	v_pk_mul_f32 v[58:59], v[58:59], 0.5 op_sel_hi:[1,0]
	v_fma_f32 v87, |v66|, s1, 1.0
	v_fma_f32 v89, |v67|, s1, 1.0
	v_rcp_f32_e32 v88, v87
	v_rcp_f32_e32 v89, v89
	v_mul_f32_e64 v87, |v66|, -|v66|
	v_mul_f32_e32 v87, 0x3fb8aa3b, v87
	v_exp_f32_e32 v90, v87
	v_mul_f32_e64 v87, |v67|, -|v67|
	v_pk_fma_f32 v[92:93], v[88:89], s[2:3], v[0:1] op_sel_hi:[1,0,0]
	v_mul_f32_e32 v87, 0x3fb8aa3b, v87
	v_pk_fma_f32 v[92:93], v[88:89], v[92:93], s[8:9] op_sel_hi:[1,1,0]
	v_exp_f32_e32 v91, v87
	v_pk_fma_f32 v[92:93], v[88:89], v[92:93], s[0:1] op_sel_hi:[1,1,0]
	v_pk_add_f32 v[42:43], v[2:3], v[42:43]
	v_pk_fma_f32 v[92:93], v[88:89], v[92:93], s[4:5] op_sel_hi:[1,1,0]
	v_pk_fma_f32 v[36:37], v[38:39], v[80:81], v[36:37] op_sel_hi:[0,1,1] neg_lo:[1,0,0] neg_hi:[1,0,0]
	v_pk_mul_f32 v[88:89], v[88:89], v[92:93]
	v_pk_fma_f32 v[36:37], v[38:39], v[36:37], v[82:83] op_sel:[1,0,0]
	v_pk_fma_f32 v[88:89], v[90:91], v[88:89], 1.0 op_sel_hi:[1,1,0] neg_lo:[1,0,0] neg_hi:[1,0,0]
	v_pk_add_f32 v[36:37], v[12:13], v[36:37]
	v_bfi_b32 v67, s3, v89, v67
	v_bfi_b32 v66, s3, v88, v66
	v_pk_add_f32 v[66:67], v[66:67], 1.0 op_sel_hi:[1,0]
	v_pk_fma_f32 v[30:31], v[38:39], v[74:75], v[30:31] op_sel_hi:[0,1,1] neg_lo:[1,0,0] neg_hi:[1,0,0]
	v_pk_mul_f32 v[58:59], v[58:59], v[66:67]
	v_pk_add_f32 v[66:67], v[106:107], v[114:115]
	v_cvt_pk_f16_f32 v128, v58, v59
	v_pk_add_f32 v[58:59], v[98:99], v[110:111]
	v_pk_fma_f32 v[30:31], v[38:39], v[30:31], v[78:79] op_sel:[1,0,0]
	v_pk_fma_f32 v[60:61], v[50:51], v[58:59], v[60:61] op_sel_hi:[0,1,1] neg_lo:[1,0,0] neg_hi:[1,0,0]
	v_pk_fma_f32 v[50:51], v[50:51], v[60:61], v[66:67] op_sel:[1,0,0]
	v_pk_fma_f32 v[44:45], v[52:53], v[58:59], v[44:45] op_sel_hi:[0,1,1] neg_lo:[1,0,0] neg_hi:[1,0,0]
	v_pk_add_f32 v[50:51], v[4:5], v[50:51]
	v_pk_fma_f32 v[44:45], v[52:53], v[44:45], v[66:67] op_sel:[1,0,0]
	v_pk_mul_f32 v[60:61], v[50:51], s[6:7] op_sel_hi:[1,0]
	v_pk_mul_f32 v[50:51], v[50:51], 0.5 op_sel_hi:[1,0]
	v_fma_f32 v87, |v60|, s1, 1.0
	v_fma_f32 v89, |v61|, s1, 1.0
	v_rcp_f32_e32 v90, v87
	v_rcp_f32_e32 v91, v89
	v_mul_f32_e64 v87, |v60|, -|v60|
	v_mul_f32_e32 v87, 0x3fb8aa3b, v87
	v_exp_f32_e32 v92, v87
	v_mul_f32_e64 v87, |v61|, -|v61|
	v_pk_fma_f32 v[94:95], v[90:91], s[2:3], v[0:1] op_sel_hi:[1,0,0]
	v_mul_f32_e32 v87, 0x3fb8aa3b, v87
	v_pk_fma_f32 v[94:95], v[90:91], v[94:95], s[8:9] op_sel_hi:[1,1,0]
	v_exp_f32_e32 v93, v87
	v_pk_fma_f32 v[94:95], v[90:91], v[94:95], s[0:1] op_sel_hi:[1,1,0]
	v_pk_add_f32 v[44:45], v[4:5], v[44:45]
	v_pk_fma_f32 v[94:95], v[90:91], v[94:95], s[4:5] op_sel_hi:[1,1,0]
	v_pk_add_f32 v[30:31], v[6:7], v[30:31]
	v_pk_mul_f32 v[90:91], v[90:91], v[94:95]
	v_pk_fma_f32 v[32:33], v[38:39], v[68:69], v[32:33] op_sel_hi:[0,1,1] neg_lo:[1,0,0] neg_hi:[1,0,0]
	v_pk_fma_f32 v[90:91], v[92:93], v[90:91], 1.0 op_sel_hi:[1,1,0] neg_lo:[1,0,0] neg_hi:[1,0,0]
	v_pk_fma_f32 v[32:33], v[38:39], v[32:33], v[70:71] op_sel:[1,0,0]
	v_bfi_b32 v61, s3, v91, v61
	v_bfi_b32 v60, s3, v90, v60
	v_pk_add_f32 v[60:61], v[60:61], 1.0 op_sel_hi:[1,0]
	v_pk_add_f32 v[32:33], v[8:9], v[32:33]
	v_pk_mul_f32 v[50:51], v[50:51], v[60:61]
	v_pk_mul_f32 v[60:61], v[54:55], s[6:7] op_sel_hi:[1,0]
	v_cvt_pk_f16_f32 v129, v50, v51
	v_fma_f32 v87, |v60|, s1, 1.0
	v_fma_f32 v89, |v61|, s1, 1.0
	v_rcp_f32_e32 v88, v87
	v_rcp_f32_e32 v89, v89
	v_mul_f32_e64 v87, |v60|, -|v60|
	v_mul_f32_e32 v87, 0x3fb8aa3b, v87
	v_exp_f32_e32 v90, v87
	v_mul_f32_e64 v87, |v61|, -|v61|
	v_pk_fma_f32 v[92:93], v[88:89], s[2:3], v[0:1] op_sel_hi:[1,0,0]
	v_mul_f32_e32 v87, 0x3fb8aa3b, v87
	v_pk_fma_f32 v[92:93], v[88:89], v[92:93], s[8:9] op_sel_hi:[1,1,0]
	v_exp_f32_e32 v91, v87
	v_pk_fma_f32 v[92:93], v[88:89], v[92:93], s[0:1] op_sel_hi:[1,1,0]
	v_pk_mul_f32 v[54:55], v[54:55], 0.5 op_sel_hi:[1,0]
	v_pk_fma_f32 v[92:93], v[88:89], v[92:93], s[4:5] op_sel_hi:[1,1,0]
	v_or_b32_e32 v50, 16, v86
	v_pk_mul_f32 v[88:89], v[88:89], v[92:93]
	v_mad_i64_i32 v[50:51], s[10:11], v50, s5, 0
	v_pk_fma_f32 v[88:89], v[90:91], v[88:89], 1.0 op_sel_hi:[1,1,0] neg_lo:[1,0,0] neg_hi:[1,0,0]
	v_lshl_add_u64 v[50:51], v[50:51], 1, s[16:17]
	v_bfi_b32 v61, s3, v89, v61
	v_bfi_b32 v60, s3, v88, v60
	v_pk_add_f32 v[60:61], v[60:61], 1.0 op_sel_hi:[1,0]
	v_lshl_add_u64 v[50:51], v[50:51], 0, v[72:73]
	v_pk_mul_f32 v[54:55], v[54:55], v[60:61]
	v_pk_mul_f32 v[60:61], v[56:57], s[6:7] op_sel_hi:[1,0]
	v_cvt_pk_f16_f32 v124, v54, v55
	v_fma_f32 v55, |v60|, s1, 1.0
	v_fma_f32 v87, |v61|, s1, 1.0
	v_rcp_f32_e32 v88, v55
	v_rcp_f32_e32 v89, v87
	v_mul_f32_e64 v55, |v60|, -|v60|
	v_mul_f32_e32 v55, 0x3fb8aa3b, v55
	v_exp_f32_e32 v90, v55
	v_mul_f32_e64 v55, |v61|, -|v61|
	v_pk_fma_f32 v[92:93], v[88:89], s[2:3], v[0:1] op_sel_hi:[1,0,0]
	v_mul_f32_e32 v55, 0x3fb8aa3b, v55
	v_pk_fma_f32 v[92:93], v[88:89], v[92:93], s[8:9] op_sel_hi:[1,1,0]
	v_exp_f32_e32 v91, v55
	v_pk_fma_f32 v[92:93], v[88:89], v[92:93], s[0:1] op_sel_hi:[1,1,0]
	v_pk_mul_f32 v[56:57], v[56:57], 0.5 op_sel_hi:[1,0]
	v_pk_fma_f32 v[92:93], v[88:89], v[92:93], s[4:5] op_sel_hi:[1,1,0]
	v_pk_fma_f32 v[26:27], v[38:39], v[62:63], v[26:27] op_sel_hi:[0,1,1] neg_lo:[1,0,0] neg_hi:[1,0,0]
	v_pk_mul_f32 v[88:89], v[88:89], v[92:93]
	v_pk_fma_f32 v[26:27], v[38:39], v[26:27], v[64:65] op_sel:[1,0,0]
	v_pk_fma_f32 v[88:89], v[90:91], v[88:89], 1.0 op_sel_hi:[1,1,0] neg_lo:[1,0,0] neg_hi:[1,0,0]
	v_pk_add_f32 v[26:27], v[2:3], v[26:27]
	v_bfi_b32 v61, s3, v89, v61
	v_bfi_b32 v60, s3, v88, v60
	v_pk_add_f32 v[60:61], v[60:61], 1.0 op_sel_hi:[1,0]
	v_pk_fma_f32 v[28:29], v[38:39], v[58:59], v[28:29] op_sel_hi:[0,1,1] neg_lo:[1,0,0] neg_hi:[1,0,0]
	v_pk_mul_f32 v[56:57], v[56:57], v[60:61]
	v_pk_fma_f32 v[28:29], v[38:39], v[28:29], v[66:67] op_sel:[1,0,0]
	v_cvt_pk_f16_f32 v125, v56, v57
	v_pk_mul_f32 v[54:55], v[46:47], s[6:7] op_sel_hi:[1,0]
	v_pk_mul_f32 v[46:47], v[46:47], 0.5 op_sel_hi:[1,0]
	v_fma_f32 v56, |v54|, s1, 1.0
	v_fma_f32 v57, |v55|, s1, 1.0
	v_rcp_f32_e32 v56, v56
	v_rcp_f32_e32 v57, v57
	v_mul_f32_e64 v60, |v54|, -|v54|
	v_mul_f32_e64 v61, |v55|, -|v55|
	v_mul_f32_e32 v60, 0x3fb8aa3b, v60
	v_pk_fma_f32 v[88:89], v[56:57], s[2:3], v[0:1] op_sel_hi:[1,0,0]
	v_mul_f32_e32 v61, 0x3fb8aa3b, v61
	v_exp_f32_e32 v60, v60
	v_pk_fma_f32 v[88:89], v[56:57], v[88:89], s[8:9] op_sel_hi:[1,1,0]
	v_exp_f32_e32 v61, v61
	v_pk_fma_f32 v[88:89], v[56:57], v[88:89], s[0:1] op_sel_hi:[1,1,0]
	v_pk_add_f32 v[28:29], v[4:5], v[28:29]
	v_pk_fma_f32 v[88:89], v[56:57], v[88:89], s[4:5] op_sel_hi:[1,1,0]
	v_pk_fma_f32 v[22:23], v[40:41], v[76:77], v[22:23] op_sel_hi:[0,1,1] neg_lo:[1,0,0] neg_hi:[1,0,0]
	v_pk_mul_f32 v[56:57], v[56:57], v[88:89]
	v_pk_fma_f32 v[22:23], v[40:41], v[22:23], v[84:85] op_sel:[1,0,0]
	v_pk_fma_f32 v[56:57], v[60:61], v[56:57], 1.0 op_sel_hi:[1,1,0] neg_lo:[1,0,0] neg_hi:[1,0,0]
	v_pk_add_f32 v[10:11], v[10:11], v[22:23]
	v_bfi_b32 v55, s3, v57, v55
	v_bfi_b32 v54, s3, v56, v54
	v_pk_add_f32 v[54:55], v[54:55], 1.0 op_sel_hi:[1,0]
	v_pk_mul_f32 v[22:23], v[10:11], s[6:7] op_sel_hi:[1,0]
	v_pk_mul_f32 v[46:47], v[46:47], v[54:55]
	v_pk_mul_f32 v[54:55], v[48:49], s[6:7] op_sel_hi:[1,0]
	v_cvt_pk_f16_f32 v126, v46, v47
	v_fma_f32 v47, |v54|, s1, 1.0
	v_fma_f32 v57, |v55|, s1, 1.0
	v_rcp_f32_e32 v56, v47
	v_rcp_f32_e32 v57, v57
	v_mul_f32_e64 v47, |v54|, -|v54|
	v_mul_f32_e32 v47, 0x3fb8aa3b, v47
	v_exp_f32_e32 v60, v47
	v_mul_f32_e64 v47, |v55|, -|v55|
	v_pk_fma_f32 v[88:89], v[56:57], s[2:3], v[0:1] op_sel_hi:[1,0,0]
	v_mul_f32_e32 v47, 0x3fb8aa3b, v47
	v_pk_fma_f32 v[88:89], v[56:57], v[88:89], s[8:9] op_sel_hi:[1,1,0]
	v_exp_f32_e32 v61, v47
	v_pk_fma_f32 v[88:89], v[56:57], v[88:89], s[0:1] op_sel_hi:[1,1,0]
	v_pk_mul_f32 v[48:49], v[48:49], 0.5 op_sel_hi:[1,0]
	v_pk_fma_f32 v[88:89], v[56:57], v[88:89], s[4:5] op_sel_hi:[1,1,0]
	v_pk_mul_f32 v[10:11], v[10:11], 0.5 op_sel_hi:[1,0]
	v_pk_mul_f32 v[56:57], v[56:57], v[88:89]
	s_nop 0
	v_pk_fma_f32 v[56:57], v[60:61], v[56:57], 1.0 op_sel_hi:[1,1,0] neg_lo:[1,0,0] neg_hi:[1,0,0]
	s_nop 0
	v_bfi_b32 v55, s3, v57, v55
	v_bfi_b32 v54, s3, v56, v54
	v_pk_add_f32 v[54:55], v[54:55], 1.0 op_sel_hi:[1,0]
	s_nop 0
	v_pk_mul_f32 v[48:49], v[48:49], v[54:55]
	s_nop 0
	v_cvt_pk_f16_f32 v127, v48, v49
	v_lshl_add_u64 v[138:139], v[50:51], 0, v[118:119]
	s_nop 1
	v_permlane16_swap_b32 v124, v126
	v_permlane16_swap_b32 v125, v127
	global_store_dwordx4 v[138:139], v[124:127], off
	v_pk_mul_f32 v[46:47], v[42:43], s[6:7] op_sel_hi:[1,0]
	v_pk_mul_f32 v[42:43], v[42:43], 0.5 op_sel_hi:[1,0]
	v_fma_f32 v48, |v46|, s1, 1.0
	v_fma_f32 v49, |v47|, s1, 1.0
	v_rcp_f32_e32 v48, v48
	v_rcp_f32_e32 v49, v49
	v_mul_f32_e64 v54, |v46|, -|v46|
	v_mul_f32_e64 v55, |v47|, -|v47|
	v_mul_f32_e32 v54, 0x3fb8aa3b, v54
	v_pk_fma_f32 v[56:57], v[48:49], s[2:3], v[0:1] op_sel_hi:[1,0,0]
	v_mul_f32_e32 v55, 0x3fb8aa3b, v55
	v_exp_f32_e32 v54, v54
	v_pk_fma_f32 v[56:57], v[48:49], v[56:57], s[8:9] op_sel_hi:[1,1,0]
	v_exp_f32_e32 v55, v55
	v_pk_fma_f32 v[56:57], v[48:49], v[56:57], s[0:1] op_sel_hi:[1,1,0]
	s_nop 0
	v_pk_fma_f32 v[56:57], v[48:49], v[56:57], s[4:5] op_sel_hi:[1,1,0]
	s_nop 0
	v_pk_mul_f32 v[48:49], v[48:49], v[56:57]
	s_nop 0
	v_pk_fma_f32 v[48:49], v[54:55], v[48:49], 1.0 op_sel_hi:[1,1,0] neg_lo:[1,0,0] neg_hi:[1,0,0]
	s_nop 0
	v_bfi_b32 v47, s3, v49, v47
	v_bfi_b32 v46, s3, v48, v46
	v_pk_add_f32 v[46:47], v[46:47], 1.0 op_sel_hi:[1,0]
	s_nop 0
	v_pk_mul_f32 v[42:43], v[42:43], v[46:47]
	v_pk_mul_f32 v[46:47], v[44:45], s[6:7] op_sel_hi:[1,0]
	v_cvt_pk_f16_f32 v130, v42, v43
	v_fma_f32 v43, |v46|, s1, 1.0
	v_fma_f32 v49, |v47|, s1, 1.0
	v_rcp_f32_e32 v48, v43
	v_rcp_f32_e32 v49, v49
	v_mul_f32_e64 v43, |v46|, -|v46|
	v_mul_f32_e32 v43, 0x3fb8aa3b, v43
	v_exp_f32_e32 v52, v43
	v_mul_f32_e64 v43, |v47|, -|v47|
	v_pk_fma_f32 v[54:55], v[48:49], s[2:3], v[0:1] op_sel_hi:[1,0,0]
	v_mul_f32_e32 v43, 0x3fb8aa3b, v43
	v_pk_fma_f32 v[54:55], v[48:49], v[54:55], s[8:9] op_sel_hi:[1,1,0]
	v_exp_f32_e32 v53, v43
	v_pk_fma_f32 v[54:55], v[48:49], v[54:55], s[0:1] op_sel_hi:[1,1,0]
	v_pk_mul_f32 v[44:45], v[44:45], 0.5 op_sel_hi:[1,0]
	v_pk_fma_f32 v[54:55], v[48:49], v[54:55], s[4:5] op_sel_hi:[1,1,0]
	s_nop 0
	v_pk_mul_f32 v[48:49], v[48:49], v[54:55]
	s_nop 0
	v_pk_fma_f32 v[48:49], v[52:53], v[48:49], 1.0 op_sel_hi:[1,1,0] neg_lo:[1,0,0] neg_hi:[1,0,0]
	s_nop 0
	v_bfi_b32 v47, s3, v49, v47
	v_bfi_b32 v46, s3, v48, v46
	v_pk_add_f32 v[46:47], v[46:47], 1.0 op_sel_hi:[1,0]
	s_nop 0
	v_pk_mul_f32 v[44:45], v[44:45], v[46:47]
	s_nop 0
	v_cvt_pk_f16_f32 v131, v44, v45
	v_pk_mul_f32 v[44:45], v[34:35], s[6:7] op_sel_hi:[1,0]
	v_lshl_add_u64 v[138:139], v[50:51], 0, v[136:137]
	s_nop 1
	v_permlane16_swap_b32 v128, v130
	v_permlane16_swap_b32 v129, v131
	global_store_dwordx4 v[138:139], v[128:131], off
	v_fma_f32 v46, |v44|, s1, 1.0
	v_fma_f32 v47, |v45|, s1, 1.0
	v_rcp_f32_e32 v46, v46
	v_rcp_f32_e32 v47, v47
	v_mul_f32_e64 v48, |v44|, -|v44|
	v_mul_f32_e64 v49, |v45|, -|v45|
	v_mul_f32_e32 v48, 0x3fb8aa3b, v48
	v_pk_fma_f32 v[50:51], v[46:47], s[2:3], v[0:1] op_sel_hi:[1,0,0]
	v_mul_f32_e32 v49, 0x3fb8aa3b, v49
	v_exp_f32_e32 v48, v48
	v_pk_fma_f32 v[50:51], v[46:47], v[50:51], s[8:9] op_sel_hi:[1,1,0]
	v_exp_f32_e32 v49, v49
	v_pk_fma_f32 v[50:51], v[46:47], v[50:51], s[0:1] op_sel_hi:[1,1,0]
	v_pk_mul_f32 v[34:35], v[34:35], 0.5 op_sel_hi:[1,0]
	v_pk_fma_f32 v[50:51], v[46:47], v[50:51], s[4:5] op_sel_hi:[1,1,0]
	v_or_b32_e32 v42, 32, v86
	v_pk_mul_f32 v[46:47], v[46:47], v[50:51]
	v_mad_i64_i32 v[42:43], s[10:11], v42, s5, 0
	v_pk_fma_f32 v[46:47], v[48:49], v[46:47], 1.0 op_sel_hi:[1,1,0] neg_lo:[1,0,0] neg_hi:[1,0,0]
	v_lshl_add_u64 v[42:43], v[42:43], 1, s[16:17]
	v_bfi_b32 v45, s3, v47, v45
	v_bfi_b32 v44, s3, v46, v44
	v_pk_add_f32 v[44:45], v[44:45], 1.0 op_sel_hi:[1,0]
	s_nop 0
	v_pk_mul_f32 v[34:35], v[34:35], v[44:45]
	v_pk_mul_f32 v[44:45], v[36:37], s[6:7] op_sel_hi:[1,0]
	v_cvt_pk_f16_f32 v120, v34, v35
	v_fma_f32 v35, |v44|, s1, 1.0
	v_fma_f32 v47, |v45|, s1, 1.0
	v_rcp_f32_e32 v46, v35
	v_rcp_f32_e32 v47, v47
	v_mul_f32_e64 v35, |v44|, -|v44|
	v_mul_f32_e32 v35, 0x3fb8aa3b, v35
	v_exp_f32_e32 v48, v35
	v_mul_f32_e64 v35, |v45|, -|v45|
	v_pk_fma_f32 v[50:51], v[46:47], s[2:3], v[0:1] op_sel_hi:[1,0,0]
	v_mul_f32_e32 v35, 0x3fb8aa3b, v35
	v_pk_fma_f32 v[50:51], v[46:47], v[50:51], s[8:9] op_sel_hi:[1,1,0]
	v_exp_f32_e32 v49, v35
	v_pk_fma_f32 v[50:51], v[46:47], v[50:51], s[0:1] op_sel_hi:[1,1,0]
	v_pk_mul_f32 v[36:37], v[36:37], 0.5 op_sel_hi:[1,0]
	v_pk_fma_f32 v[50:51], v[46:47], v[50:51], s[4:5] op_sel_hi:[1,1,0]
	s_nop 0
	v_pk_mul_f32 v[46:47], v[46:47], v[50:51]
	s_nop 0
	v_pk_fma_f32 v[46:47], v[48:49], v[46:47], 1.0 op_sel_hi:[1,1,0] neg_lo:[1,0,0] neg_hi:[1,0,0]
	s_nop 0
	v_bfi_b32 v45, s3, v47, v45
	v_bfi_b32 v44, s3, v46, v44
	v_pk_add_f32 v[44:45], v[44:45], 1.0 op_sel_hi:[1,0]
	s_nop 0
	v_pk_mul_f32 v[36:37], v[36:37], v[44:45]
	s_nop 0
	v_cvt_pk_f16_f32 v121, v36, v37
	v_lshl_add_u64 v[36:37], v[42:43], 0, v[72:73]
	v_pk_mul_f32 v[34:35], v[30:31], s[6:7] op_sel_hi:[1,0]
	v_pk_mul_f32 v[30:31], v[30:31], 0.5 op_sel_hi:[1,0]
	v_fma_f32 v42, |v34|, s1, 1.0
	v_fma_f32 v43, |v35|, s1, 1.0
	v_rcp_f32_e32 v42, v42
	v_rcp_f32_e32 v43, v43
	v_mul_f32_e64 v44, |v34|, -|v34|
	v_mul_f32_e64 v45, |v35|, -|v35|
	v_mul_f32_e32 v44, 0x3fb8aa3b, v44
	v_pk_fma_f32 v[46:47], v[42:43], s[2:3], v[0:1] op_sel_hi:[1,0,0]
	v_mul_f32_e32 v45, 0x3fb8aa3b, v45
	v_exp_f32_e32 v44, v44
	v_pk_fma_f32 v[46:47], v[42:43], v[46:47], s[8:9] op_sel_hi:[1,1,0]
	v_exp_f32_e32 v45, v45
	v_pk_fma_f32 v[46:47], v[42:43], v[46:47], s[0:1] op_sel_hi:[1,1,0]
	s_nop 0
	v_pk_fma_f32 v[46:47], v[42:43], v[46:47], s[4:5] op_sel_hi:[1,1,0]
	s_nop 0
	v_pk_mul_f32 v[42:43], v[42:43], v[46:47]
	s_nop 0
	v_pk_fma_f32 v[42:43], v[44:45], v[42:43], 1.0 op_sel_hi:[1,1,0] neg_lo:[1,0,0] neg_hi:[1,0,0]
	s_nop 0
	v_bfi_b32 v35, s3, v43, v35
	v_bfi_b32 v34, s3, v42, v34
	v_pk_add_f32 v[34:35], v[34:35], 1.0 op_sel_hi:[1,0]
	s_nop 0
	v_pk_mul_f32 v[30:31], v[30:31], v[34:35]
	v_pk_mul_f32 v[34:35], v[32:33], s[6:7] op_sel_hi:[1,0]
	v_cvt_pk_f16_f32 v122, v30, v31
	v_fma_f32 v31, |v34|, s1, 1.0
	v_fma_f32 v43, |v35|, s1, 1.0
	v_rcp_f32_e32 v42, v31
	v_rcp_f32_e32 v43, v43
	v_mul_f32_e64 v31, |v34|, -|v34|
	v_mul_f32_e32 v31, 0x3fb8aa3b, v31
	v_exp_f32_e32 v44, v31
	v_mul_f32_e64 v31, |v35|, -|v35|
	v_pk_fma_f32 v[46:47], v[42:43], s[2:3], v[0:1] op_sel_hi:[1,0,0]
	v_mul_f32_e32 v31, 0x3fb8aa3b, v31
	v_pk_fma_f32 v[46:47], v[42:43], v[46:47], s[8:9] op_sel_hi:[1,1,0]
	v_exp_f32_e32 v45, v31
	v_pk_fma_f32 v[46:47], v[42:43], v[46:47], s[0:1] op_sel_hi:[1,1,0]
	v_pk_mul_f32 v[32:33], v[32:33], 0.5 op_sel_hi:[1,0]
	v_pk_fma_f32 v[46:47], v[42:43], v[46:47], s[4:5] op_sel_hi:[1,1,0]
	s_nop 0
	v_pk_mul_f32 v[42:43], v[42:43], v[46:47]
	s_nop 0
	v_pk_fma_f32 v[42:43], v[44:45], v[42:43], 1.0 op_sel_hi:[1,1,0] neg_lo:[1,0,0] neg_hi:[1,0,0]
	s_nop 0
	v_bfi_b32 v35, s3, v43, v35
	v_bfi_b32 v34, s3, v42, v34
	v_pk_add_f32 v[34:35], v[34:35], 1.0 op_sel_hi:[1,0]
	s_nop 0
	v_pk_mul_f32 v[32:33], v[32:33], v[34:35]
	s_nop 0
	v_cvt_pk_f16_f32 v123, v32, v33
	v_lshl_add_u64 v[138:139], v[36:37], 0, v[118:119]
	s_nop 1
	v_permlane16_swap_b32 v120, v122
	v_permlane16_swap_b32 v121, v123
	global_store_dwordx4 v[138:139], v[120:123], off
	v_pk_mul_f32 v[30:31], v[26:27], s[6:7] op_sel_hi:[1,0]
	v_pk_mul_f32 v[26:27], v[26:27], 0.5 op_sel_hi:[1,0]
	v_fma_f32 v32, |v30|, s1, 1.0
	v_fma_f32 v33, |v31|, s1, 1.0
	v_rcp_f32_e32 v32, v32
	v_rcp_f32_e32 v33, v33
	v_mul_f32_e64 v34, |v30|, -|v30|
	v_mul_f32_e64 v35, |v31|, -|v31|
	v_mul_f32_e32 v34, 0x3fb8aa3b, v34
	v_pk_fma_f32 v[42:43], v[32:33], s[2:3], v[0:1] op_sel_hi:[1,0,0]
	v_mul_f32_e32 v35, 0x3fb8aa3b, v35
	v_exp_f32_e32 v34, v34
	v_pk_fma_f32 v[42:43], v[32:33], v[42:43], s[8:9] op_sel_hi:[1,1,0]
	v_exp_f32_e32 v35, v35
	v_pk_fma_f32 v[42:43], v[32:33], v[42:43], s[0:1] op_sel_hi:[1,1,0]
	s_nop 0
	v_pk_fma_f32 v[42:43], v[32:33], v[42:43], s[4:5] op_sel_hi:[1,1,0]
	s_nop 0
	v_pk_mul_f32 v[32:33], v[32:33], v[42:43]
	s_nop 0
	v_pk_fma_f32 v[32:33], v[34:35], v[32:33], 1.0 op_sel_hi:[1,1,0] neg_lo:[1,0,0] neg_hi:[1,0,0]
	s_nop 0
	v_bfi_b32 v31, s3, v33, v31
	v_bfi_b32 v30, s3, v32, v30
	v_pk_add_f32 v[30:31], v[30:31], 1.0 op_sel_hi:[1,0]
	s_nop 0
	v_pk_mul_f32 v[26:27], v[26:27], v[30:31]
	v_pk_mul_f32 v[30:31], v[28:29], s[6:7] op_sel_hi:[1,0]
	v_cvt_pk_f16_f32 v132, v26, v27
	v_fma_f32 v27, |v30|, s1, 1.0
	v_fma_f32 v33, |v31|, s1, 1.0
	v_rcp_f32_e32 v32, v27
	v_rcp_f32_e32 v33, v33
	v_mul_f32_e64 v27, |v30|, -|v30|
	v_mul_f32_e32 v27, 0x3fb8aa3b, v27
	v_exp_f32_e32 v34, v27
	v_mul_f32_e64 v27, |v31|, -|v31|
	v_pk_fma_f32 v[38:39], v[32:33], s[2:3], v[0:1] op_sel_hi:[1,0,0]
	v_mul_f32_e32 v27, 0x3fb8aa3b, v27
	v_pk_fma_f32 v[38:39], v[32:33], v[38:39], s[8:9] op_sel_hi:[1,1,0]
	v_exp_f32_e32 v35, v27
	v_pk_fma_f32 v[38:39], v[32:33], v[38:39], s[0:1] op_sel_hi:[1,1,0]
	v_pk_mul_f32 v[28:29], v[28:29], 0.5 op_sel_hi:[1,0]
	v_pk_fma_f32 v[38:39], v[32:33], v[38:39], s[4:5] op_sel_hi:[1,1,0]
	s_nop 0
	v_pk_mul_f32 v[32:33], v[32:33], v[38:39]
	s_nop 0
	v_pk_fma_f32 v[32:33], v[34:35], v[32:33], 1.0 op_sel_hi:[1,1,0] neg_lo:[1,0,0] neg_hi:[1,0,0]
	s_nop 0
	v_bfi_b32 v31, s3, v33, v31
	v_bfi_b32 v30, s3, v32, v30
	v_pk_add_f32 v[30:31], v[30:31], 1.0 op_sel_hi:[1,0]
	s_nop 0
	v_pk_mul_f32 v[28:29], v[28:29], v[30:31]
	v_mul_f32_e64 v30, |v22|, -|v22|
	v_cvt_pk_f16_f32 v133, v28, v29
	v_fma_f32 v28, |v22|, s1, 1.0
	v_fma_f32 v29, |v23|, s1, 1.0
	v_rcp_f32_e32 v28, v28
	v_rcp_f32_e32 v29, v29
	v_mul_f32_e64 v31, |v23|, -|v23|
	v_mul_f32_e32 v30, 0x3fb8aa3b, v30
	v_mul_f32_e32 v31, 0x3fb8aa3b, v31
	v_pk_fma_f32 v[32:33], v[28:29], s[2:3], v[0:1] op_sel_hi:[1,0,0]
	v_exp_f32_e32 v30, v30
	v_pk_fma_f32 v[32:33], v[28:29], v[32:33], s[8:9] op_sel_hi:[1,1,0]
	v_exp_f32_e32 v31, v31
	v_pk_fma_f32 v[32:33], v[28:29], v[32:33], s[0:1] op_sel_hi:[1,1,0]
	v_pk_fma_f32 v[32:33], v[28:29], v[32:33], s[4:5] op_sel_hi:[1,1,0]
	v_or_b32_e32 v26, 48, v86
	v_pk_mul_f32 v[28:29], v[28:29], v[32:33]
	v_mad_i64_i32 v[26:27], s[10:11], v26, s5, 0
	v_pk_fma_f32 v[28:29], v[30:31], v[28:29], 1.0 op_sel_hi:[1,1,0] neg_lo:[1,0,0] neg_hi:[1,0,0]
	v_lshl_add_u64 v[26:27], v[26:27], 1, s[16:17]
	v_bfi_b32 v23, s3, v29, v23
	v_bfi_b32 v22, s3, v28, v22
	v_pk_add_f32 v[22:23], v[22:23], 1.0 op_sel_hi:[1,0]
	s_nop 0
	v_pk_mul_f32 v[10:11], v[10:11], v[22:23]
	v_pk_fma_f32 v[22:23], v[40:41], v[80:81], v[24:25] op_sel_hi:[0,1,1] neg_lo:[1,0,0] neg_hi:[1,0,0]
	v_pk_fma_f32 v[22:23], v[40:41], v[22:23], v[82:83] op_sel:[1,0,0]
	v_cvt_pk_f16_f32 v124, v10, v11
	v_pk_add_f32 v[12:13], v[12:13], v[22:23]
	s_nop 0
	v_pk_mul_f32 v[22:23], v[12:13], s[6:7] op_sel_hi:[1,0]
	v_pk_mul_f32 v[12:13], v[12:13], 0.5 op_sel_hi:[1,0]
	v_fma_f32 v11, |v22|, s1, 1.0
	v_fma_f32 v25, |v23|, s1, 1.0
	v_rcp_f32_e32 v24, v11
	v_rcp_f32_e32 v25, v25
	v_mul_f32_e64 v11, |v22|, -|v22|
	v_mul_f32_e32 v11, 0x3fb8aa3b, v11
	v_exp_f32_e32 v28, v11
	v_mul_f32_e64 v11, |v23|, -|v23|
	v_pk_fma_f32 v[30:31], v[24:25], s[2:3], v[0:1] op_sel_hi:[1,0,0]
	v_mul_f32_e32 v11, 0x3fb8aa3b, v11
	v_pk_fma_f32 v[30:31], v[24:25], v[30:31], s[8:9] op_sel_hi:[1,1,0]
	v_exp_f32_e32 v29, v11
	v_pk_fma_f32 v[30:31], v[24:25], v[30:31], s[0:1] op_sel_hi:[1,1,0]
	s_nop 0
	v_pk_fma_f32 v[30:31], v[24:25], v[30:31], s[4:5] op_sel_hi:[1,1,0]
	s_nop 0
	v_pk_mul_f32 v[24:25], v[24:25], v[30:31]
	s_nop 0
	v_pk_fma_f32 v[24:25], v[28:29], v[24:25], 1.0 op_sel_hi:[1,1,0] neg_lo:[1,0,0] neg_hi:[1,0,0]
	s_nop 0
	v_bfi_b32 v23, s3, v25, v23
	v_bfi_b32 v22, s3, v24, v22
	v_pk_add_f32 v[22:23], v[22:23], 1.0 op_sel_hi:[1,0]
	s_nop 0
	v_pk_mul_f32 v[12:13], v[12:13], v[22:23]
	s_nop 0
	v_cvt_pk_f16_f32 v125, v12, v13
	v_lshl_add_u64 v[12:13], v[26:27], 0, v[72:73]
	v_pk_fma_f32 v[10:11], v[40:41], v[74:75], v[18:19] op_sel_hi:[0,1,1] neg_lo:[1,0,0] neg_hi:[1,0,0]
	v_pk_fma_f32 v[10:11], v[40:41], v[10:11], v[78:79] op_sel:[1,0,0]
	s_nop 0
	v_pk_add_f32 v[6:7], v[6:7], v[10:11]
	s_nop 0
	v_pk_mul_f32 v[10:11], v[6:7], s[6:7] op_sel_hi:[1,0]
	v_pk_mul_f32 v[6:7], v[6:7], 0.5 op_sel_hi:[1,0]
	v_fma_f32 v18, |v10|, s1, 1.0
	v_fma_f32 v19, |v11|, s1, 1.0
	v_rcp_f32_e32 v18, v18
	v_rcp_f32_e32 v19, v19
	v_mul_f32_e64 v22, |v10|, -|v10|
	v_mul_f32_e64 v23, |v11|, -|v11|
	v_mul_f32_e32 v22, 0x3fb8aa3b, v22
	v_pk_fma_f32 v[24:25], v[18:19], s[2:3], v[0:1] op_sel_hi:[1,0,0]
	v_mul_f32_e32 v23, 0x3fb8aa3b, v23
	v_exp_f32_e32 v22, v22
	v_pk_fma_f32 v[24:25], v[18:19], v[24:25], s[8:9] op_sel_hi:[1,1,0]
	v_exp_f32_e32 v23, v23
	v_pk_fma_f32 v[24:25], v[18:19], v[24:25], s[0:1] op_sel_hi:[1,1,0]
	s_nop 0
	v_pk_fma_f32 v[24:25], v[18:19], v[24:25], s[4:5] op_sel_hi:[1,1,0]
	s_nop 0
	v_pk_mul_f32 v[18:19], v[18:19], v[24:25]
	s_nop 0
	v_pk_fma_f32 v[18:19], v[22:23], v[18:19], 1.0 op_sel_hi:[1,1,0] neg_lo:[1,0,0] neg_hi:[1,0,0]
	s_nop 0
	v_bfi_b32 v11, s3, v19, v11
	v_bfi_b32 v10, s3, v18, v10
	v_pk_add_f32 v[10:11], v[10:11], 1.0 op_sel_hi:[1,0]
	s_nop 0
	v_pk_mul_f32 v[6:7], v[6:7], v[10:11]
	v_pk_fma_f32 v[10:11], v[40:41], v[68:69], v[20:21] op_sel_hi:[0,1,1] neg_lo:[1,0,0] neg_hi:[1,0,0]
	v_pk_fma_f32 v[10:11], v[40:41], v[10:11], v[70:71] op_sel:[1,0,0]
	v_cvt_pk_f16_f32 v126, v6, v7
	v_pk_add_f32 v[8:9], v[8:9], v[10:11]
	s_nop 0
	v_pk_mul_f32 v[10:11], v[8:9], s[6:7] op_sel_hi:[1,0]
	v_pk_mul_f32 v[8:9], v[8:9], 0.5 op_sel_hi:[1,0]
	v_fma_f32 v7, |v10|, s1, 1.0
	v_fma_f32 v19, |v11|, s1, 1.0
	v_rcp_f32_e32 v18, v7
	v_rcp_f32_e32 v19, v19
	v_mul_f32_e64 v7, |v10|, -|v10|
	v_mul_f32_e32 v7, 0x3fb8aa3b, v7
	v_exp_f32_e32 v20, v7
	v_mul_f32_e64 v7, |v11|, -|v11|
	v_pk_fma_f32 v[22:23], v[18:19], s[2:3], v[0:1] op_sel_hi:[1,0,0]
	v_mul_f32_e32 v7, 0x3fb8aa3b, v7
	v_pk_fma_f32 v[22:23], v[18:19], v[22:23], s[8:9] op_sel_hi:[1,1,0]
	v_exp_f32_e32 v21, v7
	v_pk_fma_f32 v[22:23], v[18:19], v[22:23], s[0:1] op_sel_hi:[1,1,0]
	s_nop 0
	v_pk_fma_f32 v[22:23], v[18:19], v[22:23], s[4:5] op_sel_hi:[1,1,0]
	s_nop 0
	v_pk_mul_f32 v[18:19], v[18:19], v[22:23]
	s_nop 0
	v_pk_fma_f32 v[18:19], v[20:21], v[18:19], 1.0 op_sel_hi:[1,1,0] neg_lo:[1,0,0] neg_hi:[1,0,0]
	s_nop 0
	v_bfi_b32 v11, s3, v19, v11
	v_bfi_b32 v10, s3, v18, v10
	v_pk_add_f32 v[10:11], v[10:11], 1.0 op_sel_hi:[1,0]
	s_nop 0
	v_pk_mul_f32 v[8:9], v[8:9], v[10:11]
	s_nop 0
	v_cvt_pk_f16_f32 v127, v8, v9
	v_lshl_add_u64 v[138:139], v[12:13], 0, v[118:119]
	s_nop 1
	v_permlane16_swap_b32 v124, v126
	v_permlane16_swap_b32 v125, v127
	global_store_dwordx4 v[138:139], v[124:127], off
	v_pk_fma_f32 v[6:7], v[40:41], v[62:63], v[14:15] op_sel_hi:[0,1,1] neg_lo:[1,0,0] neg_hi:[1,0,0]
	v_pk_fma_f32 v[6:7], v[40:41], v[6:7], v[64:65] op_sel:[1,0,0]
	s_nop 0
	v_pk_add_f32 v[2:3], v[2:3], v[6:7]
	s_nop 0
	v_pk_mul_f32 v[6:7], v[2:3], s[6:7] op_sel_hi:[1,0]
	v_pk_mul_f32 v[2:3], v[2:3], 0.5 op_sel_hi:[1,0]
	v_fma_f32 v8, |v6|, s1, 1.0
	v_fma_f32 v9, |v7|, s1, 1.0
	v_rcp_f32_e32 v8, v8
	v_rcp_f32_e32 v9, v9
	v_mul_f32_e64 v10, |v6|, -|v6|
	v_mul_f32_e64 v11, |v7|, -|v7|
	v_mul_f32_e32 v10, 0x3fb8aa3b, v10
	v_pk_fma_f32 v[14:15], v[8:9], s[2:3], v[0:1] op_sel_hi:[1,0,0]
	v_mul_f32_e32 v11, 0x3fb8aa3b, v11
	v_exp_f32_e32 v10, v10
	v_pk_fma_f32 v[14:15], v[8:9], v[14:15], s[8:9] op_sel_hi:[1,1,0]
	v_exp_f32_e32 v11, v11
	v_pk_fma_f32 v[14:15], v[8:9], v[14:15], s[0:1] op_sel_hi:[1,1,0]
	s_nop 0
	v_pk_fma_f32 v[14:15], v[8:9], v[14:15], s[4:5] op_sel_hi:[1,1,0]
	s_nop 0
	v_pk_mul_f32 v[8:9], v[8:9], v[14:15]
	s_nop 0
	v_pk_fma_f32 v[8:9], v[10:11], v[8:9], 1.0 op_sel_hi:[1,1,0] neg_lo:[1,0,0] neg_hi:[1,0,0]
	s_nop 0
	v_bfi_b32 v7, s3, v9, v7
	v_bfi_b32 v6, s3, v8, v6
	v_pk_add_f32 v[6:7], v[6:7], 1.0 op_sel_hi:[1,0]
	s_nop 0
	v_pk_mul_f32 v[2:3], v[2:3], v[6:7]
	v_pk_fma_f32 v[6:7], v[40:41], v[58:59], v[16:17] op_sel_hi:[0,1,1] neg_lo:[1,0,0] neg_hi:[1,0,0]
	v_pk_fma_f32 v[6:7], v[40:41], v[6:7], v[66:67] op_sel:[1,0,0]
	v_cvt_pk_f16_f32 v134, v2, v3
	v_pk_add_f32 v[4:5], v[4:5], v[6:7]
	s_nop 0
	v_pk_mul_f32 v[6:7], v[4:5], s[6:7] op_sel_hi:[1,0]
	v_pk_mul_f32 v[4:5], v[4:5], 0.5 op_sel_hi:[1,0]
	v_fma_f32 v3, |v6|, s1, 1.0
	v_fma_f32 v9, |v7|, s1, 1.0
	v_rcp_f32_e32 v8, v3
	v_rcp_f32_e32 v9, v9
	v_mul_f32_e64 v3, |v6|, -|v6|
	v_mul_f32_e32 v3, 0x3fb8aa3b, v3
	v_exp_f32_e32 v10, v3
	v_mul_f32_e64 v3, |v7|, -|v7|
	v_pk_fma_f32 v[0:1], v[8:9], s[2:3], v[0:1] op_sel_hi:[1,0,0]
	v_mul_f32_e32 v3, 0x3fb8aa3b, v3
	v_pk_fma_f32 v[0:1], v[8:9], v[0:1], s[8:9] op_sel_hi:[1,1,0]
	v_exp_f32_e32 v11, v3
	v_pk_fma_f32 v[0:1], v[8:9], v[0:1], s[0:1] op_sel_hi:[1,1,0]
	s_nop 0
	v_pk_fma_f32 v[0:1], v[8:9], v[0:1], s[4:5] op_sel_hi:[1,1,0]
	s_nop 0
	v_pk_mul_f32 v[0:1], v[8:9], v[0:1]
	s_nop 0
	v_pk_fma_f32 v[0:1], v[10:11], v[0:1], 1.0 op_sel_hi:[1,1,0] neg_lo:[1,0,0] neg_hi:[1,0,0]
	s_nop 0
	v_bfi_b32 v1, s3, v1, v7
	v_bfi_b32 v0, s3, v0, v6
	v_pk_add_f32 v[0:1], v[0:1], 1.0 op_sel_hi:[1,0]
	s_nop 0
	v_pk_mul_f32 v[0:1], v[4:5], v[0:1]
	s_nop 0
	v_cvt_pk_f16_f32 v135, v0, v1
	v_lshl_add_u64 v[138:139], v[12:13], 0, v[136:137]
	s_nop 1
	v_permlane16_swap_b32 v132, v134
	v_permlane16_swap_b32 v133, v135
	global_store_dwordx4 v[138:139], v[132:135], off
	s_endpgm
	.p2align	8

	.amdhsa_kernel _Z7gemm_tnILi128ELi192ELi2ELi4ELi3ELi6ELi1EEvPKDF16_S1_PKfPfPDF16_iiiiiS3_S3_S4_
		.amdhsa_group_segment_fixed_size 8192
		.amdhsa_private_segment_fixed_size 0
		.amdhsa_kernarg_size 88
		.amdhsa_user_sgpr_count 2
		.amdhsa_user_sgpr_dispatch_ptr 0
		.amdhsa_user_sgpr_queue_ptr 0
		.amdhsa_user_sgpr_kernarg_segment_ptr 1
		.amdhsa_user_sgpr_dispatch_id 0
		.amdhsa_user_sgpr_kernarg_preload_length 0
		.amdhsa_user_sgpr_kernarg_preload_offset 0
		.amdhsa_user_sgpr_private_segment_size 0
		.amdhsa_uses_dynamic_stack 0
		.amdhsa_enable_private_segment 0
		.amdhsa_system_sgpr_workgroup_id_x 1
		.amdhsa_system_sgpr_workgroup_id_y 0
		.amdhsa_system_sgpr_workgroup_id_z 0
		.amdhsa_system_sgpr_workgroup_info 0
		.amdhsa_system_vgpr_workitem_id 0
		.amdhsa_next_free_vgpr 140
		.amdhsa_next_free_sgpr 48
		.amdhsa_accum_offset 140
		.amdhsa_reserve_vcc 1
		.amdhsa_float_round_mode_32 0
		.amdhsa_float_round_mode_16_64 0
		.amdhsa_float_denorm_mode_32 3
		.amdhsa_float_denorm_mode_16_64 3
		.amdhsa_dx10_clamp 1
		.amdhsa_ieee_mode 1
		.amdhsa_fp16_overflow 0
		.amdhsa_tg_split 0
		.amdhsa_exception_fp_ieee_invalid_op 0
		.amdhsa_exception_fp_denorm_src 0
		.amdhsa_exception_fp_ieee_div_zero 0
		.amdhsa_exception_fp_ieee_overflow 0
		.amdhsa_exception_fp_ieee_underflow 0
		.amdhsa_exception_fp_ieee_inexact 0
		.amdhsa_exception_int_div_zero 0
	.end_amdhsa_kernel

amdhsa.kernels:
  - .agpr_count:     0
    .args:
      - .actual_access:  read_only
        .address_space:  global
        .offset:         0
        .size:           8
        .value_kind:     global_buffer
      - .actual_access:  write_only
        .address_space:  global
        .offset:         8
        .size:           8
        .value_kind:     global_buffer
      - .offset:         16
        .size:           4
        .value_kind:     by_value
      - .offset:         20
        .size:           4
        .value_kind:     by_value
      - .offset:         24
        .size:           4
        .value_kind:     by_value
    .group_segment_fixed_size: 17408
    .kernarg_segment_align: 8
    .kernarg_segment_size: 28
    .language:       OpenCL C
    .language_version:
      - 2
      - 0
    .max_flat_workgroup_size: 256
    .name:           _Z13conv_w_kernelPKfPDF16_iii
    .private_segment_fixed_size: 0
    .sgpr_count:     23
    .sgpr_spill_count: 0
    .symbol:         _Z13conv_w_kernelPKfPDF16_iii.kd
    .uniform_work_group_size: 1
    .uses_dynamic_stack: false
    .vgpr_count:     52
    .vgpr_spill_count: 0
    .wavefront_size: 64
  - .agpr_count:     0
    .args:
      - .offset:         0
        .size:           264
        .value_kind:     by_value
    .group_segment_fixed_size: 17408
    .kernarg_segment_align: 8
    .kernarg_segment_size: 264
    .language:       OpenCL C
    .language_version:
      - 2
      - 0
    .max_flat_workgroup_size: 256
    .name:           _Z15conv_all_kernel7ConvJob
    .private_segment_fixed_size: 0
    .sgpr_count:     78
    .sgpr_spill_count: 0
    .symbol:         _Z15conv_all_kernel7ConvJob.kd
    .uniform_work_group_size: 1
    .uses_dynamic_stack: false
    .vgpr_count:     62
    .vgpr_spill_count: 0
    .wavefront_size: 64
  - .agpr_count:     0
    .args:
      - .actual_access:  read_only
        .address_space:  global
        .offset:         0
        .size:           8
        .value_kind:     global_buffer
      - .actual_access:  read_only
        .address_space:  global
        .offset:         8
        .size:           8
        .value_kind:     global_buffer
      - .actual_access:  read_only
        .address_space:  global
        .offset:         16
        .size:           8
        .value_kind:     global_buffer
      - .actual_access:  read_only
        .address_space:  global
        .offset:         24
        .size:           8
        .value_kind:     global_buffer
      - .actual_access:  read_only
        .address_space:  global
        .offset:         32
        .size:           8
        .value_kind:     global_buffer
      - .actual_access:  write_only
        .address_space:  global
        .offset:         40
        .size:           8
        .value_kind:     global_buffer
      - .actual_access:  write_only
        .address_space:  global
        .offset:         48
        .size:           8
        .value_kind:     global_buffer
      - .offset:         56
        .size:           264
        .value_kind:     by_value
    .group_segment_fixed_size: 17408
    .kernarg_segment_align: 8
    .kernarg_segment_size: 320
    .language:       OpenCL C
    .language_version:
      - 2
      - 0
    .max_flat_workgroup_size: 256
    .name:           _Z15embed_ln_kernelPKiPKfS2_S2_S2_PfPDF16_7ConvJob
    .private_segment_fixed_size: 0
    .sgpr_count:     74
    .sgpr_spill_count: 0
    .symbol:         _Z15embed_ln_kernelPKiPKfS2_S2_S2_PfPDF16_7ConvJob.kd
    .uniform_work_group_size: 1
    .uses_dynamic_stack: false
    .vgpr_count:     62
    .vgpr_spill_count: 0
    .wavefront_size: 64
  - .agpr_count:     0
    .args:
      - .actual_access:  read_only
        .address_space:  global
        .offset:         0
        .size:           8
        .value_kind:     global_buffer
      - .actual_access:  read_only
        .address_space:  global
        .offset:         8
        .size:           8
        .value_kind:     global_buffer
      - .actual_access:  read_only
        .address_space:  global
        .offset:         16
        .size:           8
        .value_kind:     global_buffer
      - .actual_access:  write_only
        .address_space:  global
        .offset:         24
        .size:           8
        .value_kind:     global_buffer
      - .offset:         32
        .size:           264
        .value_kind:     by_value
    .group_segment_fixed_size: 17408
    .kernarg_segment_align: 8
    .kernarg_segment_size: 296
    .language:       OpenCL C
    .language_version:
      - 2
      - 0
    .max_flat_workgroup_size: 256
    .name:           _Z9ln_kernelPKfS0_S0_PDF16_7ConvJob
    .private_segment_fixed_size: 0
    .sgpr_count:     74
    .sgpr_spill_count: 0
    .symbol:         _Z9ln_kernelPKfS0_S0_PDF16_7ConvJob.kd
    .uniform_work_group_size: 1
    .uses_dynamic_stack: false
    .vgpr_count:     62
    .vgpr_spill_count: 0
    .wavefront_size: 64
  - .agpr_count:     0
    .args:
      - .actual_access:  read_only
        .address_space:  global
        .offset:         0
        .size:           8
        .value_kind:     global_buffer
      - .actual_access:  write_only
        .address_space:  global
        .offset:         8
        .size:           8
        .value_kind:     global_buffer
      - .offset:         16
        .size:           264
        .value_kind:     by_value
    .group_segment_fixed_size: 35072
    .kernarg_segment_align: 8
    .kernarg_segment_size: 280
    .language:       OpenCL C
    .language_version:
      - 2
      - 0
    .max_flat_workgroup_size: 512
    .name:           _Z18attn_rowsum_kernelPKDF16_PDF16_7ConvJob
    .private_segment_fixed_size: 0
    .sgpr_count:     74
    .sgpr_spill_count: 0
    .symbol:         _Z18attn_rowsum_kernelPKDF16_PDF16_7ConvJob.kd
    .uniform_work_group_size: 1
    .uses_dynamic_stack: false
    .vgpr_count:     72
    .vgpr_spill_count: 0
    .wavefront_size: 64
  - .agpr_count:     0
    .args:
      - .actual_access:  read_only
        .address_space:  global
        .offset:         0
        .size:           8
        .value_kind:     global_buffer
      - .actual_access:  read_only
        .address_space:  global
        .offset:         8
        .size:           8
        .value_kind:     global_buffer
      - .actual_access:  read_only
        .address_space:  global
        .offset:         16
        .size:           8
        .value_kind:     global_buffer
      - .address_space:  global
        .offset:         24
        .size:           8
        .value_kind:     global_buffer
      - .actual_access:  write_only
        .address_space:  global
        .offset:         32
        .size:           8
        .value_kind:     global_buffer
      - .offset:         40
        .size:           4
        .value_kind:     by_value
      - .offset:         44
        .size:           4
        .value_kind:     by_value
      - .offset:         48
        .size:           4
        .value_kind:     by_value
      - .offset:         52
        .size:           4
        .value_kind:     by_value
      - .offset:         56
        .size:           4
        .value_kind:     by_value
      - .actual_access:  read_only
        .address_space:  global
        .offset:         64
        .size:           8
        .value_kind:     global_buffer
      - .actual_access:  read_only
        .address_space:  global
        .offset:         72
        .size:           8
        .value_kind:     global_buffer
      - .address_space:  global
        .offset:         80
        .size:           8
        .value_kind:     global_buffer
    .group_segment_fixed_size: 0
    .kernarg_segment_align: 8
    .kernarg_segment_size: 88
    .language:       OpenCL C
    .language_version:
      - 2
      - 0
    .max_flat_workgroup_size: 768
    .name:           _Z7gemm_tnILi128ELi144ELi4ELi3ELi4ELi0ELi1EEvPKDF16_S1_PKfPfPDF16_iiiiiS3_S3_S4_
    .private_segment_fixed_size: 0
    .sgpr_count:     37
    .sgpr_spill_count: 0
    .symbol:         _Z7gemm_tnILi128ELi144ELi4ELi3ELi4ELi0ELi1EEvPKDF16_S1_PKfPfPDF16_iiiiiS3_S3_S4_.kd
    .uniform_work_group_size: 1
    .uses_dynamic_stack: false
    .vgpr_count:     68
    .vgpr_spill_count: 0
    .wavefront_size: 64
  - .agpr_count:     0
    .args:
      - .actual_access:  read_only
        .address_space:  global
        .offset:         0
        .size:           8
        .value_kind:     global_buffer
      - .actual_access:  read_only
        .address_space:  global
        .offset:         8
        .size:           8
        .value_kind:     global_buffer
      - .actual_access:  read_only
        .address_space:  global
        .offset:         16
        .size:           8
        .value_kind:     global_buffer
      - .address_space:  global
        .offset:         24
        .size:           8
        .value_kind:     global_buffer
      - .actual_access:  write_only
        .address_space:  global
        .offset:         32
        .size:           8
        .value_kind:     global_buffer
      - .offset:         40
        .size:           4
        .value_kind:     by_value
      - .offset:         44
        .size:           4
        .value_kind:     by_value
      - .offset:         48
        .size:           4
        .value_kind:     by_value
      - .offset:         52
        .size:           4
        .value_kind:     by_value
      - .offset:         56
        .size:           4
        .value_kind:     by_value
      - .actual_access:  read_only
        .address_space:  global
        .offset:         64
        .size:           8
        .value_kind:     global_buffer
      - .actual_access:  read_only
        .address_space:  global
        .offset:         72
        .size:           8
        .value_kind:     global_buffer
      - .address_space:  global
        .offset:         80
        .size:           8
        .value_kind:     global_buffer
    .group_segment_fixed_size: 7424
    .kernarg_segment_align: 8
    .kernarg_segment_size: 88
    .language:       OpenCL C
    .language_version:
      - 2
      - 0
    .max_flat_workgroup_size: 768
    .name:           _Z7gemm_tnILi128ELi144ELi4ELi3ELi4ELi7ELi1EEvPKDF16_S1_PKfPfPDF16_iiiiiS3_S3_S4_
    .private_segment_fixed_size: 0
    .sgpr_count:     46
    .sgpr_spill_count: 0
    .symbol:         _Z7gemm_tnILi128ELi144ELi4ELi3ELi4ELi7ELi1EEvPKDF16_S1_PKfPfPDF16_iiiiiS3_S3_S4_.kd
    .uniform_work_group_size: 1
    .uses_dynamic_stack: false
    .vgpr_count:     100
    .vgpr_spill_count: 0
    .wavefront_size: 64
  - .agpr_count:     24
    .args:
      - .actual_access:  read_only
        .address_space:  global
        .offset:         0
        .size:           8
        .value_kind:     global_buffer
      - .actual_access:  read_only
        .address_space:  global
        .offset:         8
        .size:           8
        .value_kind:     global_buffer
      - .actual_access:  read_only
        .address_space:  global
        .offset:         16
        .size:           8
        .value_kind:     global_buffer
      - .address_space:  global
        .offset:         24
        .size:           8
        .value_kind:     global_buffer
      - .actual_access:  read_only
        .address_space:  global
        .offset:         32
        .size:           8
        .value_kind:     global_buffer
      - .offset:         40
        .size:           4
        .value_kind:     by_value
      - .offset:         44
        .size:           4
        .value_kind:     by_value
      - .offset:         48
        .size:           4
        .value_kind:     by_value
      - .offset:         52
        .size:           4
        .value_kind:     by_value
      - .offset:         56
        .size:           4
        .value_kind:     by_value
      - .actual_access:  read_only
        .address_space:  global
        .offset:         64
        .size:           8
        .value_kind:     global_buffer
      - .actual_access:  read_only
        .address_space:  global
        .offset:         72
        .size:           8
        .value_kind:     global_buffer
      - .address_space:  global
        .offset:         80
        .size:           8
        .value_kind:     global_buffer
    .group_segment_fixed_size: 0
    .kernarg_segment_align: 8
    .kernarg_segment_size: 88
    .language:       OpenCL C
    .language_version:
      - 2
      - 0
    .max_flat_workgroup_size: 256
    .name:           _Z7gemm_tnILi64ELi96ELi2ELi2ELi8ELi2ELi1EEvPKDF16_S1_PKfPfPDF16_iiiiiS3_S3_S4_
    .private_segment_fixed_size: 0
    .sgpr_count:     46
    .sgpr_spill_count: 0
    .symbol:         _Z7gemm_tnILi64ELi96ELi2ELi2ELi8ELi2ELi1EEvPKDF16_S1_PKfPfPDF16_iiiiiS3_S3_S4_.kd
    .uniform_work_group_size: 1
    .uses_dynamic_stack: false
    .vgpr_count:     100
    .vgpr_spill_count: 0
    .wavefront_size: 64
  - .agpr_count:     0
    .args:
      - .actual_access:  read_only
        .address_space:  global
        .offset:         0
        .size:           8
        .value_kind:     global_buffer
      - .actual_access:  read_only
        .address_space:  global
        .offset:         8
        .size:           8
        .value_kind:     global_buffer
      - .actual_access:  read_only
        .address_space:  global
        .offset:         16
        .size:           8
        .value_kind:     global_buffer
      - .address_space:  global
        .offset:         24
        .size:           8
        .value_kind:     global_buffer
      - .actual_access:  write_only
        .address_space:  global
        .offset:         32
        .size:           8
        .value_kind:     global_buffer
      - .offset:         40
        .size:           4
        .value_kind:     by_value
      - .offset:         44
        .size:           4
        .value_kind:     by_value
      - .offset:         48
        .size:           4
        .value_kind:     by_value
      - .offset:         52
        .size:           4
        .value_kind:     by_value
      - .offset:         56
        .size:           4
        .value_kind:     by_value
      - .actual_access:  read_only
        .address_space:  global
        .offset:         64
        .size:           8
        .value_kind:     global_buffer
      - .actual_access:  read_only
        .address_space:  global
        .offset:         72
        .size:           8
        .value_kind:     global_buffer
      - .address_space:  global
        .offset:         80
        .size:           8
        .value_kind:     global_buffer
    .group_segment_fixed_size: 8192
    .kernarg_segment_align: 8
    .kernarg_segment_size: 88
    .language:       OpenCL C
    .language_version:
      - 2
      - 0
    .max_flat_workgroup_size: 512
    .name:           _Z7gemm_tnILi128ELi192ELi2ELi4ELi3ELi6ELi1EEvPKDF16_S1_PKfPfPDF16_iiiiiS3_S3_S4_
    .private_segment_fixed_size: 0
    .sgpr_count:     54
    .sgpr_spill_count: 0
    .symbol:         _Z7gemm_tnILi128ELi192ELi2ELi4ELi3ELi6ELi1EEvPKDF16_S1_PKfPfPDF16_iiiiiS3_S3_S4_.kd
    .uniform_work_group_size: 1
    .uses_dynamic_stack: false
    .vgpr_count:     140
    .vgpr_spill_count: 0
    .wavefront_size: 64
  - .agpr_count:     24
    .args:
      - .actual_access:  read_only
        .address_space:  global
        .offset:         0
        .size:           8
        .value_kind:     global_buffer
      - .actual_access:  read_only
        .address_space:  global
        .offset:         8
        .size:           8
        .value_kind:     global_buffer
      - .actual_access:  read_only
        .address_space:  global
        .offset:         16
        .size:           8
        .value_kind:     global_buffer
      - .address_space:  global
        .offset:         24
        .size:           8
        .value_kind:     global_buffer
      - .actual_access:  write_only
        .address_space:  global
        .offset:         32
        .size:           8
        .value_kind:     global_buffer
      - .offset:         40
        .size:           4
        .value_kind:     by_value
      - .offset:         44
        .size:           4
        .value_kind:     by_value
      - .offset:         48
        .size:           4
        .value_kind:     by_value
      - .offset:         52
        .size:           4
        .value_kind:     by_value
      - .offset:         56
        .size:           4
        .value_kind:     by_value
      - .actual_access:  read_only
        .address_space:  global
        .offset:         64
        .size:           8
        .value_kind:     global_buffer
      - .actual_access:  read_only
        .address_space:  global
        .offset:         72
        .size:           8
        .value_kind:     global_buffer
      - .address_space:  global
        .offset:         80
        .size:           8
        .value_kind:     global_buffer
    .group_segment_fixed_size: 0
    .kernarg_segment_align: 8
    .kernarg_segment_size: 88
    .language:       OpenCL C
    .language_version:
      - 2
      - 0
    .max_flat_workgroup_size: 256
    .name:           _Z7gemm_tnILi64ELi96ELi2ELi2ELi8ELi5ELi1EEvPKDF16_S1_PKfPfPDF16_iiiiiS3_S3_S4_
    .private_segment_fixed_size: 0
    .sgpr_count:     52
    .sgpr_spill_count: 0
    .symbol:         _Z7gemm_tnILi64ELi96ELi2ELi2ELi8ELi5ELi1EEvPKDF16_S1_PKfPfPDF16_iiiiiS3_S3_S4_.kd
    .uniform_work_group_size: 1
    .uses_dynamic_stack: false
    .vgpr_count:     128
    .vgpr_spill_count: 0
    .wavefront_size: 64
  - .agpr_count:     0
    .args:
      - .actual_access:  read_only
        .address_space:  global
        .offset:         0
        .size:           8
        .value_kind:     global_buffer
      - .actual_access:  read_only
        .address_space:  global
        .offset:         8
        .size:           8
        .value_kind:     global_buffer
      - .actual_access:  read_only
        .address_space:  global
        .offset:         16
        .size:           8
        .value_kind:     global_buffer
      - .address_space:  global
        .offset:         24
        .size:           8
        .value_kind:     global_buffer
      - .actual_access:  read_only
        .address_space:  global
        .offset:         32
        .size:           8
        .value_kind:     global_buffer
      - .offset:         40
        .size:           4
        .value_kind:     by_value
      - .offset:         44
        .size:           4
        .value_kind:     by_value
      - .offset:         48
        .size:           4
        .value_kind:     by_value
      - .offset:         52
        .size:           4
        .value_kind:     by_value
      - .offset:         56
        .size:           4
        .value_kind:     by_value
      - .actual_access:  read_only
        .address_space:  global
        .offset:         64
        .size:           8
        .value_kind:     global_buffer
      - .actual_access:  read_only
        .address_space:  global
        .offset:         72
        .size:           8
        .value_kind:     global_buffer
      - .address_space:  global
        .offset:         80
        .size:           8
        .value_kind:     global_buffer
    .group_segment_fixed_size: 0
    .kernarg_segment_align: 8
    .kernarg_segment_size: 88
    .language:       OpenCL C
    .language_version:
      - 2
      - 0
    .max_flat_workgroup_size: 512
    .name:           _Z7gemm_tnILi128ELi192ELi2ELi4ELi3ELi3ELi4EEvPKDF16_S1_PKfPfPDF16_iiiiiS3_S3_S4_
    .private_segment_fixed_size: 0
    .sgpr_count:     40
    .sgpr_spill_count: 0
    .symbol:         _Z7gemm_tnILi128ELi192ELi2ELi4ELi3ELi3ELi4EEvPKDF16_S1_PKfPfPDF16_iiiiiS3_S3_S4_.kd
    .uniform_work_group_size: 1
    .uses_dynamic_stack: false
    .vgpr_count:     102
    .vgpr_spill_count: 0
    .wavefront_size: 64
  - .agpr_count:     0
    .args:
      - .address_space:  global
        .offset:         0
        .size:           8
        .value_kind:     global_buffer
      - .address_space:  global
        .offset:         8
        .size:           8
        .value_kind:     global_buffer
      - .address_space:  global
        .offset:         16
        .size:           8
        .value_kind:     global_buffer
      - .offset:         24
        .size:           4
        .value_kind:     by_value
      - .offset:         28
        .size:           4
        .value_kind:     by_value
      - .offset:         32
        .size:           4
        .value_kind:     by_value
      - .offset:         36
        .size:           4
        .value_kind:     by_value
      - .offset:         40
        .size:           4
        .value_kind:     by_value
    .group_segment_fixed_size: 0
    .kernarg_segment_align: 8
    .kernarg_segment_size: 44
    .language:       OpenCL C
    .language_version:
      - 2
      - 0
    .max_flat_workgroup_size: 512
    .name:           _Z17gemm_256sq_8phaseILi0EEvPKDF16_S1_Pfiiiii
    .private_segment_fixed_size: 0
    .sgpr_count:     48
    .sgpr_spill_count: 0
    .symbol:         _Z17gemm_256sq_8phaseILi0EEvPKDF16_S1_Pfiiiii.kd
    .uniform_work_group_size: 1
    .uses_dynamic_stack: false
    .vgpr_count:     244
    .vgpr_spill_count: 0
    .wavefront_size: 64
